# in-proj and down-GEMM epilogues: dropped dead zero-initialisations of fp8 pack registers (both words are written by the convert pair)
# baseline (speedup 1.0000x reference)
.LBB0_196:
	s_ashr_i32 s33, s7, 31
	v_readlane_b32 s57, v253, 35
	s_add_u32 s57, s57, s7
	v_readlane_b32 s59, v253, 37
	s_addc_u32 s33, s59, s33
	v_readlane_b32 s59, v253, 39
	s_add_u32 s59, s59, s7
	v_readlane_b32 s66, v253, 41
	s_addc_u32 s66, s66, 0
	s_add_u32 s59, s59, 0xfffffc00
	s_addc_u32 s66, s66, -1
	v_pk_mul_f32 v[10:11], v[158:159], s[12:13] op_sel_hi:[1,0]
	s_cmp_lt_i32 s0, 4
	v_med3_f32 v16, v10, s52, v179
	v_med3_f32 v11, v11, s52, v179
	s_cselect_b32 s67, s33, s66
	s_cselect_b32 s66, s57, s59
	v_cvt_pk_fp8_f32 v10, v16, v11
	v_lshl_add_u64 v[6:7], s[66:67], 0, v[4:5]
	v_lshlrev_b64 v[8:9], 10, v[2:3]
	v_lshl_add_u64 v[6:7], v[6:7], 0, v[8:9]
	v_lshrrev_b32_e32 v214, 6, v0
	v_lshlrev_b32_e32 v214, 13, v214
	v_and_b32_e32 v215, 63, v0
	v_lshl_add_u32 v214, v215, 3, v214
	v_lshrrev_b32_e32 v215, 8, v2
	v_lshl_add_u32 v214, v215, 18, v214
	s_sub_i32 s32, s7, 0x400
	s_cmp_lt_i32 s0, 4
	s_cselect_b32 s32, s7, s32
	s_mulk_i32 s32, 0xff
	v_add_u32_e32 v214, s32, v214
	v_mov_b32_e32 v215, 0
	v_lshl_add_u64 v[220:221], s[66:67], 0, v[214:215]
	v_add_co_u32_e32 v222, vcc, 0x1000, v220
	s_nop 1
	v_addc_co_u32_e32 v223, vcc, 0, v221, vcc
	v_pk_mul_f32 v[8:9], v[160:161], s[12:13] op_sel_hi:[1,0]
	v_pk_mul_f32 v[14:15], v[154:155], s[12:13] op_sel_hi:[1,0]
	v_med3_f32 v8, v8, s52, v179
	v_med3_f32 v9, v9, s52, v179
	v_cvt_pk_fp8_f32 v10, v8, v9 op_sel:[0,0,1]
	v_med3_f32 v8, v14, s52, v179
	v_med3_f32 v9, v15, s52, v179
	v_cvt_pk_fp8_f32 v11, v8, v9
	v_pk_mul_f32 v[12:13], v[156:157], s[12:13] op_sel_hi:[1,0]
	v_pk_mul_f32 v[14:15], v[142:143], s[12:13] op_sel_hi:[1,0]
	v_med3_f32 v8, v12, s52, v179
	v_med3_f32 v9, v13, s52, v179
	v_cvt_pk_fp8_f32 v11, v8, v9 op_sel:[0,0,1]
	v_pk_mul_f32 v[8:9], v[152:153], s[12:13] op_sel_hi:[1,0]
	v_pk_mul_f32 v[12:13], v[144:145], s[12:13] op_sel_hi:[1,0]
	v_med3_f32 v8, v8, s52, v179
	global_store_dwordx2 v[220:221], v[10:11], off
	v_pk_mul_f32 v[10:11], v[150:151], s[12:13] op_sel_hi:[1,0]
	v_med3_f32 v9, v9, s52, v179
	v_med3_f32 v16, v10, s52, v179
	v_med3_f32 v11, v11, s52, v179
	v_cvt_pk_fp8_f32 v10, v16, v11
	v_pk_mul_f32 v[16:17], v[138:139], s[12:13] op_sel_hi:[1,0]
	s_movk_i32 s0, 0x4000
	v_cvt_pk_fp8_f32 v10, v8, v9 op_sel:[0,0,1]
	v_med3_f32 v8, v14, s52, v179
	v_med3_f32 v9, v15, s52, v179
	v_cvt_pk_fp8_f32 v11, v8, v9
	v_med3_f32 v8, v12, s52, v179
	v_med3_f32 v9, v13, s52, v179
	v_pk_mul_f32 v[12:13], v[146:147], s[12:13] op_sel_hi:[1,0]
	v_cvt_pk_fp8_f32 v11, v8, v9 op_sel:[0,0,1]
	v_med3_f32 v18, v12, s52, v179
	v_med3_f32 v13, v13, s52, v179
	v_cvt_pk_fp8_f32 v12, v18, v13
	global_store_dwordx2 v[220:221], v[10:11], off offset:512
	v_pk_mul_f32 v[10:11], v[148:149], s[12:13] op_sel_hi:[1,0]
	v_mov_b32_e32 v13, 0
	v_med3_f32 v10, v10, s52, v179
	v_med3_f32 v11, v11, s52, v179
	v_cvt_pk_fp8_f32 v12, v10, v11 op_sel:[0,0,1]
	v_med3_f32 v10, v16, s52, v179
	v_med3_f32 v11, v17, s52, v179
	v_cvt_pk_fp8_f32 v13, v10, v11
	v_pk_mul_f32 v[14:15], v[140:141], s[12:13] op_sel_hi:[1,0]
	v_pk_mul_f32 v[16:17], v[126:127], s[12:13] op_sel_hi:[1,0]
	v_med3_f32 v10, v14, s52, v179
	v_med3_f32 v11, v15, s52, v179
	v_cvt_pk_fp8_f32 v13, v10, v11 op_sel:[0,0,1]
	v_add_co_u32_e32 v10, vcc, s0, v6
	v_pk_mul_f32 v[14:15], v[128:129], s[12:13] op_sel_hi:[1,0]
	s_nop 0
	v_addc_co_u32_e32 v11, vcc, 0, v7, vcc
	global_store_dwordx2 v[220:221], v[12:13], off offset:1024
	v_pk_mul_f32 v[12:13], v[134:135], s[12:13] op_sel_hi:[1,0]
	v_pk_mul_f32 v[10:11], v[136:137], s[12:13] op_sel_hi:[1,0]
	v_med3_f32 v18, v12, s52, v179
	v_med3_f32 v13, v13, s52, v179
	v_cvt_pk_fp8_f32 v12, v18, v13
	v_med3_f32 v10, v10, s52, v179
	v_med3_f32 v11, v11, s52, v179
	v_cvt_pk_fp8_f32 v12, v10, v11 op_sel:[0,0,1]
	v_med3_f32 v10, v16, s52, v179
	v_med3_f32 v11, v17, s52, v179
	v_cvt_pk_fp8_f32 v13, v10, v11
	v_med3_f32 v10, v14, s52, v179
	v_med3_f32 v11, v15, s52, v179
	v_lshl_add_u64 v[8:9], v[6:7], 0, s[14:15]
	v_cvt_pk_fp8_f32 v13, v10, v11 op_sel:[0,0,1]
	v_pk_mul_f32 v[10:11], v[132:133], s[12:13] op_sel_hi:[1,0]
	v_pk_mul_f32 v[16:17], v[122:123], s[12:13] op_sel_hi:[1,0]
	v_med3_f32 v10, v10, s52, v179
	global_store_dwordx2 v[220:221], v[12:13], off offset:1536
	v_pk_mul_f32 v[12:13], v[130:131], s[12:13] op_sel_hi:[1,0]
	v_med3_f32 v11, v11, s52, v179
	v_med3_f32 v18, v12, s52, v179
	v_med3_f32 v13, v13, s52, v179
	v_cvt_pk_fp8_f32 v12, v18, v13
	v_pk_mul_f32 v[14:15], v[124:125], s[12:13] op_sel_hi:[1,0]
	s_mov_b32 s0, 0x8000
	v_cvt_pk_fp8_f32 v12, v10, v11 op_sel:[0,0,1]
	v_med3_f32 v10, v16, s52, v179
	v_med3_f32 v11, v17, s52, v179
	v_cvt_pk_fp8_f32 v13, v10, v11
	v_med3_f32 v10, v14, s52, v179
	v_med3_f32 v11, v15, s52, v179
	v_pk_mul_f32 v[16:17], v[110:111], s[12:13] op_sel_hi:[1,0]
	v_cvt_pk_fp8_f32 v13, v10, v11 op_sel:[0,0,1]
	v_add_co_u32_e32 v10, vcc, s0, v6
	v_pk_mul_f32 v[14:15], v[112:113], s[12:13] op_sel_hi:[1,0]
	s_nop 0
	v_addc_co_u32_e32 v11, vcc, 0, v7, vcc
	global_store_dwordx2 v[220:221], v[12:13], off offset:2048
	v_pk_mul_f32 v[12:13], v[118:119], s[12:13] op_sel_hi:[1,0]
	v_pk_mul_f32 v[10:11], v[120:121], s[12:13] op_sel_hi:[1,0]
	v_med3_f32 v18, v12, s52, v179
	v_med3_f32 v13, v13, s52, v179
	v_cvt_pk_fp8_f32 v12, v18, v13
	v_med3_f32 v10, v10, s52, v179
	v_med3_f32 v11, v11, s52, v179
	v_cvt_pk_fp8_f32 v12, v10, v11 op_sel:[0,0,1]
	v_med3_f32 v10, v16, s52, v179
	v_med3_f32 v11, v17, s52, v179
	v_cvt_pk_fp8_f32 v13, v10, v11
	v_med3_f32 v10, v14, s52, v179
	v_med3_f32 v11, v15, s52, v179
	v_lshl_add_u64 v[8:9], v[6:7], 0, s[16:17]
	v_cvt_pk_fp8_f32 v13, v10, v11 op_sel:[0,0,1]
	v_pk_mul_f32 v[10:11], v[116:117], s[12:13] op_sel_hi:[1,0]
	v_pk_mul_f32 v[16:17], v[106:107], s[12:13] op_sel_hi:[1,0]
	v_med3_f32 v10, v10, s52, v179
	global_store_dwordx2 v[220:221], v[12:13], off offset:2560
	v_pk_mul_f32 v[12:13], v[114:115], s[12:13] op_sel_hi:[1,0]
	v_med3_f32 v11, v11, s52, v179
	v_med3_f32 v18, v12, s52, v179
	v_med3_f32 v13, v13, s52, v179
	v_cvt_pk_fp8_f32 v12, v18, v13
	v_pk_mul_f32 v[14:15], v[108:109], s[12:13] op_sel_hi:[1,0]
	v_lshl_add_u64 v[8:9], v[6:7], 0, s[18:19]
	v_cvt_pk_fp8_f32 v12, v10, v11 op_sel:[0,0,1]
	v_med3_f32 v10, v16, s52, v179
	v_med3_f32 v11, v17, s52, v179
	v_cvt_pk_fp8_f32 v13, v10, v11
	v_med3_f32 v10, v14, s52, v179
	v_med3_f32 v11, v15, s52, v179
	v_pk_mul_f32 v[16:17], v[98:99], s[12:13] op_sel_hi:[1,0]
	v_cvt_pk_fp8_f32 v13, v10, v11 op_sel:[0,0,1]
	v_add_co_u32_e32 v10, vcc, s91, v6
	v_pk_mul_f32 v[14:15], v[100:101], s[12:13] op_sel_hi:[1,0]
	s_nop 0
	v_addc_co_u32_e32 v11, vcc, 0, v7, vcc
	global_store_dwordx2 v[220:221], v[12:13], off offset:3072
	v_pk_mul_f32 v[12:13], v[102:103], s[12:13] op_sel_hi:[1,0]
	v_pk_mul_f32 v[10:11], v[104:105], s[12:13] op_sel_hi:[1,0]
	v_med3_f32 v18, v12, s52, v179
	v_med3_f32 v13, v13, s52, v179
	v_cvt_pk_fp8_f32 v12, v18, v13
	v_med3_f32 v10, v10, s52, v179
	v_med3_f32 v11, v11, s52, v179
	v_cvt_pk_fp8_f32 v12, v10, v11 op_sel:[0,0,1]
	v_med3_f32 v10, v16, s52, v179
	v_med3_f32 v11, v17, s52, v179
	v_cvt_pk_fp8_f32 v13, v10, v11
	v_med3_f32 v10, v14, s52, v179
	v_med3_f32 v11, v15, s52, v179
	v_pk_mul_f32 v[16:17], v[90:91], s[12:13] op_sel_hi:[1,0]
	v_cvt_pk_fp8_f32 v13, v10, v11 op_sel:[0,0,1]
	v_pk_mul_f32 v[10:11], v[96:97], s[12:13] op_sel_hi:[1,0]
	v_pk_mul_f32 v[14:15], v[92:93], s[12:13] op_sel_hi:[1,0]
	v_med3_f32 v10, v10, s52, v179
	global_store_dwordx2 v[220:221], v[12:13], off offset:3584
	v_pk_mul_f32 v[12:13], v[94:95], s[12:13] op_sel_hi:[1,0]
	v_med3_f32 v11, v11, s52, v179
	v_med3_f32 v18, v12, s52, v179
	v_med3_f32 v13, v13, s52, v179
	v_cvt_pk_fp8_f32 v12, v18, v13
	s_mov_b64 s[66:67], 0x20000
	v_lshl_add_u64 v[8:9], v[6:7], 0, s[66:67]
	v_cvt_pk_fp8_f32 v12, v10, v11 op_sel:[0,0,1]
	v_med3_f32 v10, v16, s52, v179
	v_med3_f32 v11, v17, s52, v179
	v_cvt_pk_fp8_f32 v13, v10, v11
	v_med3_f32 v10, v14, s52, v179
	v_med3_f32 v11, v15, s52, v179
	v_pk_mul_f32 v[16:17], v[78:79], s[12:13] op_sel_hi:[1,0]
	v_cvt_pk_fp8_f32 v13, v10, v11 op_sel:[0,0,1]
	v_add_co_u32_e32 v10, vcc, s53, v6
	v_pk_mul_f32 v[14:15], v[80:81], s[12:13] op_sel_hi:[1,0]
	s_nop 0
	v_addc_co_u32_e32 v11, vcc, 0, v7, vcc
	global_store_dwordx2 v[222:223], v[12:13], off
	v_pk_mul_f32 v[12:13], v[86:87], s[12:13] op_sel_hi:[1,0]
	v_pk_mul_f32 v[10:11], v[88:89], s[12:13] op_sel_hi:[1,0]
	v_med3_f32 v18, v12, s52, v179
	v_med3_f32 v13, v13, s52, v179
	v_cvt_pk_fp8_f32 v12, v18, v13
	v_med3_f32 v10, v10, s52, v179
	v_med3_f32 v11, v11, s52, v179
	v_cvt_pk_fp8_f32 v12, v10, v11 op_sel:[0,0,1]
	v_med3_f32 v10, v16, s52, v179
	v_med3_f32 v11, v17, s52, v179
	v_cvt_pk_fp8_f32 v13, v10, v11
	v_med3_f32 v10, v14, s52, v179
	v_med3_f32 v11, v15, s52, v179
	v_pk_mul_f32 v[16:17], v[74:75], s[12:13] op_sel_hi:[1,0]
	v_cvt_pk_fp8_f32 v13, v10, v11 op_sel:[0,0,1]
	v_pk_mul_f32 v[10:11], v[84:85], s[12:13] op_sel_hi:[1,0]
	v_pk_mul_f32 v[14:15], v[76:77], s[12:13] op_sel_hi:[1,0]
	v_med3_f32 v10, v10, s52, v179
	global_store_dwordx2 v[222:223], v[12:13], off offset:512
	v_pk_mul_f32 v[12:13], v[82:83], s[12:13] op_sel_hi:[1,0]
	v_med3_f32 v11, v11, s52, v179
	v_med3_f32 v18, v12, s52, v179
	v_med3_f32 v13, v13, s52, v179
	v_cvt_pk_fp8_f32 v12, v18, v13
	v_mov_b32_e32 v13, 0
	v_lshl_add_u64 v[8:9], v[6:7], 0, s[20:21]
	v_cvt_pk_fp8_f32 v12, v10, v11 op_sel:[0,0,1]
	v_med3_f32 v10, v16, s52, v179
	v_med3_f32 v11, v17, s52, v179
	v_cvt_pk_fp8_f32 v13, v10, v11
	v_med3_f32 v10, v14, s52, v179
	v_med3_f32 v11, v15, s52, v179
	v_pk_mul_f32 v[16:17], v[62:63], s[12:13] op_sel_hi:[1,0]
	v_cvt_pk_fp8_f32 v13, v10, v11 op_sel:[0,0,1]
	v_add_co_u32_e32 v10, vcc, s64, v6
	v_pk_mul_f32 v[14:15], v[64:65], s[12:13] op_sel_hi:[1,0]
	s_nop 0
	v_addc_co_u32_e32 v11, vcc, 0, v7, vcc
	global_store_dwordx2 v[222:223], v[12:13], off offset:1024
	v_pk_mul_f32 v[12:13], v[70:71], s[12:13] op_sel_hi:[1,0]
	v_pk_mul_f32 v[10:11], v[72:73], s[12:13] op_sel_hi:[1,0]
	v_med3_f32 v18, v12, s52, v179
	v_med3_f32 v13, v13, s52, v179
	v_cvt_pk_fp8_f32 v12, v18, v13
	v_med3_f32 v10, v10, s52, v179
	v_med3_f32 v11, v11, s52, v179
	v_cvt_pk_fp8_f32 v12, v10, v11 op_sel:[0,0,1]
	v_med3_f32 v10, v16, s52, v179
	v_med3_f32 v11, v17, s52, v179
	v_cvt_pk_fp8_f32 v13, v10, v11
	v_med3_f32 v10, v14, s52, v179
	v_med3_f32 v11, v15, s52, v179
	v_pk_mul_f32 v[16:17], v[58:59], s[12:13] op_sel_hi:[1,0]
	v_cvt_pk_fp8_f32 v13, v10, v11 op_sel:[0,0,1]
	v_pk_mul_f32 v[10:11], v[68:69], s[12:13] op_sel_hi:[1,0]
	v_pk_mul_f32 v[14:15], v[60:61], s[12:13] op_sel_hi:[1,0]
	v_med3_f32 v10, v10, s52, v179
	global_store_dwordx2 v[222:223], v[12:13], off offset:1536
	v_pk_mul_f32 v[12:13], v[66:67], s[12:13] op_sel_hi:[1,0]
	v_med3_f32 v11, v11, s52, v179
	v_med3_f32 v18, v12, s52, v179
	v_med3_f32 v13, v13, s52, v179
	v_cvt_pk_fp8_f32 v12, v18, v13
	v_mov_b32_e32 v13, 0
	v_lshl_add_u64 v[8:9], v[6:7], 0, s[22:23]
	v_cvt_pk_fp8_f32 v12, v10, v11 op_sel:[0,0,1]
	v_med3_f32 v10, v16, s52, v179
	v_med3_f32 v11, v17, s52, v179
	v_cvt_pk_fp8_f32 v13, v10, v11
	v_med3_f32 v10, v14, s52, v179
	v_med3_f32 v11, v15, s52, v179
	v_pk_mul_f32 v[16:17], v[46:47], s[12:13] op_sel_hi:[1,0]
	v_cvt_pk_fp8_f32 v13, v10, v11 op_sel:[0,0,1]
	v_add_co_u32_e32 v10, vcc, s65, v6
	v_pk_mul_f32 v[14:15], v[48:49], s[12:13] op_sel_hi:[1,0]
	s_nop 0
	v_addc_co_u32_e32 v11, vcc, 0, v7, vcc
	global_store_dwordx2 v[222:223], v[12:13], off offset:2048
	v_pk_mul_f32 v[12:13], v[54:55], s[12:13] op_sel_hi:[1,0]
	v_pk_mul_f32 v[10:11], v[56:57], s[12:13] op_sel_hi:[1,0]
	v_med3_f32 v18, v12, s52, v179
	v_med3_f32 v13, v13, s52, v179
	v_cvt_pk_fp8_f32 v12, v18, v13
	v_med3_f32 v10, v10, s52, v179
	v_med3_f32 v11, v11, s52, v179
	v_cvt_pk_fp8_f32 v12, v10, v11 op_sel:[0,0,1]
	v_med3_f32 v10, v16, s52, v179
	v_med3_f32 v11, v17, s52, v179
	v_cvt_pk_fp8_f32 v13, v10, v11
	v_med3_f32 v10, v14, s52, v179
	v_med3_f32 v11, v15, s52, v179
	v_pk_mul_f32 v[16:17], v[42:43], s[12:13] op_sel_hi:[1,0]
	v_cvt_pk_fp8_f32 v13, v10, v11 op_sel:[0,0,1]
	v_pk_mul_f32 v[10:11], v[52:53], s[12:13] op_sel_hi:[1,0]
	v_pk_mul_f32 v[14:15], v[44:45], s[12:13] op_sel_hi:[1,0]
	v_med3_f32 v10, v10, s52, v179
	global_store_dwordx2 v[222:223], v[12:13], off offset:2560
	v_pk_mul_f32 v[12:13], v[50:51], s[12:13] op_sel_hi:[1,0]
	v_med3_f32 v11, v11, s52, v179
	v_med3_f32 v18, v12, s52, v179
	v_med3_f32 v13, v13, s52, v179
	v_cvt_pk_fp8_f32 v12, v18, v13
	v_lshl_add_u64 v[8:9], v[6:7], 0, s[40:41]
	v_add_co_u32_e32 v6, vcc, s31, v6
	v_cvt_pk_fp8_f32 v12, v10, v11 op_sel:[0,0,1]
	v_med3_f32 v10, v16, s52, v179
	v_med3_f32 v11, v17, s52, v179
	v_cvt_pk_fp8_f32 v13, v10, v11
	v_med3_f32 v10, v14, s52, v179
	v_med3_f32 v11, v15, s52, v179
	v_addc_co_u32_e32 v7, vcc, 0, v7, vcc
	v_cvt_pk_fp8_f32 v13, v10, v11 op_sel:[0,0,1]
	v_pk_mul_f32 v[10:11], v[38:39], s[12:13] op_sel_hi:[1,0]
	v_pk_mul_f32 v[14:15], v[34:35], s[12:13] op_sel_hi:[1,0]
	v_med3_f32 v16, v10, s52, v179
	v_med3_f32 v11, v11, s52, v179
	v_cvt_pk_fp8_f32 v10, v16, v11
	global_store_dwordx2 v[222:223], v[12:13], off offset:3072
	v_pk_mul_f32 v[6:7], v[40:41], s[12:13] op_sel_hi:[1,0]
	v_mov_b32_e32 v11, 0
	v_med3_f32 v6, v6, s52, v179
	v_med3_f32 v7, v7, s52, v179
	v_cvt_pk_fp8_f32 v10, v6, v7 op_sel:[0,0,1]
	v_med3_f32 v6, v14, s52, v179
	v_med3_f32 v7, v15, s52, v179
	v_cvt_pk_fp8_f32 v11, v6, v7
	v_pk_mul_f32 v[12:13], v[36:37], s[12:13] op_sel_hi:[1,0]
	s_nop 0
	v_med3_f32 v6, v12, s52, v179
	v_med3_f32 v7, v13, s52, v179
	v_cvt_pk_fp8_f32 v11, v6, v7 op_sel:[0,0,1]
	global_store_dwordx2 v[222:223], v[10:11], off offset:3584
	s_cbranch_execnz .LBB0_195

.LBB0_223:
	s_ashr_i32 s7, s4, 31
	v_readlane_b32 s29, v253, 35
	s_add_u32 s29, s29, s4
	v_readlane_b32 s33, v253, 37
	s_addc_u32 s7, s33, s7
	v_readlane_b32 s33, v253, 39
	s_add_u32 s33, s33, s4
	v_readlane_b32 s57, v253, 41
	s_addc_u32 s57, s57, 0
	s_add_u32 s33, s33, 0xfffffc00
	s_addc_u32 s57, s57, -1
	v_pk_mul_f32 v[10:11], v[158:159], s[12:13] op_sel_hi:[1,0]
	s_cmp_lt_i32 s76, 4
	v_med3_f32 v16, v10, s52, v175
	v_med3_f32 v11, v11, s52, v175
	s_cselect_b32 s79, s7, s57
	s_cselect_b32 s78, s29, s33
	v_cvt_pk_fp8_f32 v10, v16, v11
	v_lshl_add_u64 v[6:7], s[78:79], 0, v[4:5]
	v_lshlrev_b64 v[8:9], 10, v[2:3]
	v_lshl_add_u64 v[6:7], v[6:7], 0, v[8:9]
	v_lshrrev_b32_e32 v214, 6, v0
	v_lshlrev_b32_e32 v214, 13, v214
	v_and_b32_e32 v215, 63, v0
	v_lshl_add_u32 v214, v215, 3, v214
	v_lshrrev_b32_e32 v215, 8, v2
	v_lshl_add_u32 v214, v215, 18, v214
	s_sub_i32 s32, s4, 0x400
	s_cmp_lt_i32 s76, 4
	s_cselect_b32 s32, s4, s32
	s_mulk_i32 s32, 0xff
	v_add_u32_e32 v214, s32, v214
	v_mov_b32_e32 v215, 0
	v_lshl_add_u64 v[220:221], s[78:79], 0, v[214:215]
	v_add_co_u32_e32 v222, vcc, 0x1000, v220
	s_nop 1
	v_addc_co_u32_e32 v223, vcc, 0, v221, vcc
	v_pk_mul_f32 v[8:9], v[160:161], s[12:13] op_sel_hi:[1,0]
	v_pk_mul_f32 v[14:15], v[154:155], s[12:13] op_sel_hi:[1,0]
	v_med3_f32 v8, v8, s52, v175
	v_med3_f32 v9, v9, s52, v175
	v_cvt_pk_fp8_f32 v10, v8, v9 op_sel:[0,0,1]
	v_med3_f32 v8, v14, s52, v175
	v_med3_f32 v9, v15, s52, v175
	v_cvt_pk_fp8_f32 v11, v8, v9
	v_pk_mul_f32 v[12:13], v[156:157], s[12:13] op_sel_hi:[1,0]
	v_pk_mul_f32 v[14:15], v[142:143], s[12:13] op_sel_hi:[1,0]
	v_med3_f32 v8, v12, s52, v175
	v_med3_f32 v9, v13, s52, v175
	v_cvt_pk_fp8_f32 v11, v8, v9 op_sel:[0,0,1]
	v_pk_mul_f32 v[8:9], v[152:153], s[12:13] op_sel_hi:[1,0]
	v_pk_mul_f32 v[12:13], v[144:145], s[12:13] op_sel_hi:[1,0]
	v_med3_f32 v8, v8, s52, v175
	global_store_dwordx2 v[220:221], v[10:11], off
	v_pk_mul_f32 v[10:11], v[150:151], s[12:13] op_sel_hi:[1,0]
	v_med3_f32 v9, v9, s52, v175
	v_med3_f32 v16, v10, s52, v175
	v_med3_f32 v11, v11, s52, v175
	v_cvt_pk_fp8_f32 v10, v16, v11
	v_pk_mul_f32 v[16:17], v[138:139], s[12:13] op_sel_hi:[1,0]
	s_movk_i32 s7, 0x4000
	v_cvt_pk_fp8_f32 v10, v8, v9 op_sel:[0,0,1]
	v_med3_f32 v8, v14, s52, v175
	v_med3_f32 v9, v15, s52, v175
	v_cvt_pk_fp8_f32 v11, v8, v9
	v_med3_f32 v8, v12, s52, v175
	v_med3_f32 v9, v13, s52, v175
	v_pk_mul_f32 v[12:13], v[146:147], s[12:13] op_sel_hi:[1,0]
	v_cvt_pk_fp8_f32 v11, v8, v9 op_sel:[0,0,1]
	v_med3_f32 v18, v12, s52, v175
	v_med3_f32 v13, v13, s52, v175
	v_cvt_pk_fp8_f32 v12, v18, v13
	global_store_dwordx2 v[220:221], v[10:11], off offset:512
	v_pk_mul_f32 v[10:11], v[148:149], s[12:13] op_sel_hi:[1,0]
	v_mov_b32_e32 v13, 0
	v_med3_f32 v10, v10, s52, v175
	v_med3_f32 v11, v11, s52, v175
	v_cvt_pk_fp8_f32 v12, v10, v11 op_sel:[0,0,1]
	v_med3_f32 v10, v16, s52, v175
	v_med3_f32 v11, v17, s52, v175
	v_cvt_pk_fp8_f32 v13, v10, v11
	v_pk_mul_f32 v[14:15], v[140:141], s[12:13] op_sel_hi:[1,0]
	v_pk_mul_f32 v[16:17], v[126:127], s[12:13] op_sel_hi:[1,0]
	v_med3_f32 v10, v14, s52, v175
	v_med3_f32 v11, v15, s52, v175
	v_cvt_pk_fp8_f32 v13, v10, v11 op_sel:[0,0,1]
	v_add_co_u32_e32 v10, vcc, s7, v6
	v_pk_mul_f32 v[14:15], v[128:129], s[12:13] op_sel_hi:[1,0]
	s_nop 0
	v_addc_co_u32_e32 v11, vcc, 0, v7, vcc
	global_store_dwordx2 v[220:221], v[12:13], off offset:1024
	v_pk_mul_f32 v[12:13], v[134:135], s[12:13] op_sel_hi:[1,0]
	v_pk_mul_f32 v[10:11], v[136:137], s[12:13] op_sel_hi:[1,0]
	v_med3_f32 v18, v12, s52, v175
	v_med3_f32 v13, v13, s52, v175
	v_cvt_pk_fp8_f32 v12, v18, v13
	v_med3_f32 v10, v10, s52, v175
	v_med3_f32 v11, v11, s52, v175
	v_cvt_pk_fp8_f32 v12, v10, v11 op_sel:[0,0,1]
	v_med3_f32 v10, v16, s52, v175
	v_med3_f32 v11, v17, s52, v175
	v_cvt_pk_fp8_f32 v13, v10, v11
	v_med3_f32 v10, v14, s52, v175
	v_med3_f32 v11, v15, s52, v175
	v_lshl_add_u64 v[8:9], v[6:7], 0, s[14:15]
	v_cvt_pk_fp8_f32 v13, v10, v11 op_sel:[0,0,1]
	v_pk_mul_f32 v[10:11], v[132:133], s[12:13] op_sel_hi:[1,0]
	v_pk_mul_f32 v[16:17], v[122:123], s[12:13] op_sel_hi:[1,0]
	v_med3_f32 v10, v10, s52, v175
	global_store_dwordx2 v[220:221], v[12:13], off offset:1536
	v_pk_mul_f32 v[12:13], v[130:131], s[12:13] op_sel_hi:[1,0]
	v_med3_f32 v11, v11, s52, v175
	v_med3_f32 v18, v12, s52, v175
	v_med3_f32 v13, v13, s52, v175
	v_cvt_pk_fp8_f32 v12, v18, v13
	v_pk_mul_f32 v[14:15], v[124:125], s[12:13] op_sel_hi:[1,0]
	s_mov_b32 s7, 0x8000
	v_cvt_pk_fp8_f32 v12, v10, v11 op_sel:[0,0,1]
	v_med3_f32 v10, v16, s52, v175
	v_med3_f32 v11, v17, s52, v175
	v_cvt_pk_fp8_f32 v13, v10, v11
	v_med3_f32 v10, v14, s52, v175
	v_med3_f32 v11, v15, s52, v175
	v_pk_mul_f32 v[16:17], v[110:111], s[12:13] op_sel_hi:[1,0]
	v_cvt_pk_fp8_f32 v13, v10, v11 op_sel:[0,0,1]
	v_add_co_u32_e32 v10, vcc, s7, v6
	v_pk_mul_f32 v[14:15], v[112:113], s[12:13] op_sel_hi:[1,0]
	s_nop 0
	v_addc_co_u32_e32 v11, vcc, 0, v7, vcc
	global_store_dwordx2 v[220:221], v[12:13], off offset:2048
	v_pk_mul_f32 v[12:13], v[118:119], s[12:13] op_sel_hi:[1,0]
	v_pk_mul_f32 v[10:11], v[120:121], s[12:13] op_sel_hi:[1,0]
	v_med3_f32 v18, v12, s52, v175
	v_med3_f32 v13, v13, s52, v175
	v_cvt_pk_fp8_f32 v12, v18, v13
	v_med3_f32 v10, v10, s52, v175
	v_med3_f32 v11, v11, s52, v175
	v_cvt_pk_fp8_f32 v12, v10, v11 op_sel:[0,0,1]
	v_med3_f32 v10, v16, s52, v175
	v_med3_f32 v11, v17, s52, v175
	v_cvt_pk_fp8_f32 v13, v10, v11
	v_med3_f32 v10, v14, s52, v175
	v_med3_f32 v11, v15, s52, v175
	v_lshl_add_u64 v[8:9], v[6:7], 0, s[16:17]
	v_cvt_pk_fp8_f32 v13, v10, v11 op_sel:[0,0,1]
	v_pk_mul_f32 v[10:11], v[116:117], s[12:13] op_sel_hi:[1,0]
	v_pk_mul_f32 v[16:17], v[106:107], s[12:13] op_sel_hi:[1,0]
	v_med3_f32 v10, v10, s52, v175
	global_store_dwordx2 v[220:221], v[12:13], off offset:2560
	v_pk_mul_f32 v[12:13], v[114:115], s[12:13] op_sel_hi:[1,0]
	v_med3_f32 v11, v11, s52, v175
	v_med3_f32 v18, v12, s52, v175
	v_med3_f32 v13, v13, s52, v175
	v_cvt_pk_fp8_f32 v12, v18, v13
	v_pk_mul_f32 v[14:15], v[108:109], s[12:13] op_sel_hi:[1,0]
	v_lshl_add_u64 v[8:9], v[6:7], 0, s[18:19]
	v_cvt_pk_fp8_f32 v12, v10, v11 op_sel:[0,0,1]
	v_med3_f32 v10, v16, s52, v175
	v_med3_f32 v11, v17, s52, v175
	v_cvt_pk_fp8_f32 v13, v10, v11
	v_med3_f32 v10, v14, s52, v175
	v_med3_f32 v11, v15, s52, v175
	v_pk_mul_f32 v[16:17], v[98:99], s[12:13] op_sel_hi:[1,0]
	v_cvt_pk_fp8_f32 v13, v10, v11 op_sel:[0,0,1]
	v_add_co_u32_e32 v10, vcc, s96, v6
	v_pk_mul_f32 v[14:15], v[100:101], s[12:13] op_sel_hi:[1,0]
	s_nop 0
	v_addc_co_u32_e32 v11, vcc, 0, v7, vcc
	global_store_dwordx2 v[220:221], v[12:13], off offset:3072
	v_pk_mul_f32 v[12:13], v[102:103], s[12:13] op_sel_hi:[1,0]
	v_pk_mul_f32 v[10:11], v[104:105], s[12:13] op_sel_hi:[1,0]
	v_med3_f32 v18, v12, s52, v175
	v_med3_f32 v13, v13, s52, v175
	v_cvt_pk_fp8_f32 v12, v18, v13
	v_med3_f32 v10, v10, s52, v175
	v_med3_f32 v11, v11, s52, v175
	v_cvt_pk_fp8_f32 v12, v10, v11 op_sel:[0,0,1]
	v_med3_f32 v10, v16, s52, v175
	v_med3_f32 v11, v17, s52, v175
	v_cvt_pk_fp8_f32 v13, v10, v11
	v_med3_f32 v10, v14, s52, v175
	v_med3_f32 v11, v15, s52, v175
	v_pk_mul_f32 v[16:17], v[90:91], s[12:13] op_sel_hi:[1,0]
	v_cvt_pk_fp8_f32 v13, v10, v11 op_sel:[0,0,1]
	v_pk_mul_f32 v[10:11], v[96:97], s[12:13] op_sel_hi:[1,0]
	v_pk_mul_f32 v[14:15], v[92:93], s[12:13] op_sel_hi:[1,0]
	v_med3_f32 v10, v10, s52, v175
	global_store_dwordx2 v[220:221], v[12:13], off offset:3584
	v_pk_mul_f32 v[12:13], v[94:95], s[12:13] op_sel_hi:[1,0]
	v_med3_f32 v11, v11, s52, v175
	v_med3_f32 v18, v12, s52, v175
	v_med3_f32 v13, v13, s52, v175
	v_cvt_pk_fp8_f32 v12, v18, v13
	s_mov_b64 s[78:79], 0x20000
	v_lshl_add_u64 v[8:9], v[6:7], 0, s[78:79]
	v_cvt_pk_fp8_f32 v12, v10, v11 op_sel:[0,0,1]
	v_med3_f32 v10, v16, s52, v175
	v_med3_f32 v11, v17, s52, v175
	v_cvt_pk_fp8_f32 v13, v10, v11
	v_med3_f32 v10, v14, s52, v175
	v_med3_f32 v11, v15, s52, v175
	v_pk_mul_f32 v[16:17], v[78:79], s[12:13] op_sel_hi:[1,0]
	v_cvt_pk_fp8_f32 v13, v10, v11 op_sel:[0,0,1]
	v_add_co_u32_e32 v10, vcc, s53, v6
	v_pk_mul_f32 v[14:15], v[80:81], s[12:13] op_sel_hi:[1,0]
	s_nop 0
	v_addc_co_u32_e32 v11, vcc, 0, v7, vcc
	global_store_dwordx2 v[222:223], v[12:13], off
	v_pk_mul_f32 v[12:13], v[86:87], s[12:13] op_sel_hi:[1,0]
	v_pk_mul_f32 v[10:11], v[88:89], s[12:13] op_sel_hi:[1,0]
	v_med3_f32 v18, v12, s52, v175
	v_med3_f32 v13, v13, s52, v175
	v_cvt_pk_fp8_f32 v12, v18, v13
	v_med3_f32 v10, v10, s52, v175
	v_med3_f32 v11, v11, s52, v175
	v_cvt_pk_fp8_f32 v12, v10, v11 op_sel:[0,0,1]
	v_med3_f32 v10, v16, s52, v175
	v_med3_f32 v11, v17, s52, v175
	v_cvt_pk_fp8_f32 v13, v10, v11
	v_med3_f32 v10, v14, s52, v175
	v_med3_f32 v11, v15, s52, v175
	v_pk_mul_f32 v[16:17], v[74:75], s[12:13] op_sel_hi:[1,0]
	v_cvt_pk_fp8_f32 v13, v10, v11 op_sel:[0,0,1]
	v_pk_mul_f32 v[10:11], v[84:85], s[12:13] op_sel_hi:[1,0]
	v_pk_mul_f32 v[14:15], v[76:77], s[12:13] op_sel_hi:[1,0]
	v_med3_f32 v10, v10, s52, v175
	global_store_dwordx2 v[222:223], v[12:13], off offset:512
	v_pk_mul_f32 v[12:13], v[82:83], s[12:13] op_sel_hi:[1,0]
	v_med3_f32 v11, v11, s52, v175
	v_med3_f32 v18, v12, s52, v175
	v_med3_f32 v13, v13, s52, v175
	v_cvt_pk_fp8_f32 v12, v18, v13
	v_mov_b32_e32 v13, 0
	v_lshl_add_u64 v[8:9], v[6:7], 0, s[20:21]
	v_cvt_pk_fp8_f32 v12, v10, v11 op_sel:[0,0,1]
	v_med3_f32 v10, v16, s52, v175
	v_med3_f32 v11, v17, s52, v175
	v_cvt_pk_fp8_f32 v13, v10, v11
	v_med3_f32 v10, v14, s52, v175
	v_med3_f32 v11, v15, s52, v175
	v_pk_mul_f32 v[16:17], v[62:63], s[12:13] op_sel_hi:[1,0]
	v_cvt_pk_fp8_f32 v13, v10, v11 op_sel:[0,0,1]
	v_add_co_u32_e32 v10, vcc, s64, v6
	v_pk_mul_f32 v[14:15], v[64:65], s[12:13] op_sel_hi:[1,0]
	s_nop 0
	v_addc_co_u32_e32 v11, vcc, 0, v7, vcc
	global_store_dwordx2 v[222:223], v[12:13], off offset:1024
	v_pk_mul_f32 v[12:13], v[70:71], s[12:13] op_sel_hi:[1,0]
	v_pk_mul_f32 v[10:11], v[72:73], s[12:13] op_sel_hi:[1,0]
	v_med3_f32 v18, v12, s52, v175
	v_med3_f32 v13, v13, s52, v175
	v_cvt_pk_fp8_f32 v12, v18, v13
	v_med3_f32 v10, v10, s52, v175
	v_med3_f32 v11, v11, s52, v175
	v_cvt_pk_fp8_f32 v12, v10, v11 op_sel:[0,0,1]
	v_med3_f32 v10, v16, s52, v175
	v_med3_f32 v11, v17, s52, v175
	v_cvt_pk_fp8_f32 v13, v10, v11
	v_med3_f32 v10, v14, s52, v175
	v_med3_f32 v11, v15, s52, v175
	v_pk_mul_f32 v[16:17], v[58:59], s[12:13] op_sel_hi:[1,0]
	v_cvt_pk_fp8_f32 v13, v10, v11 op_sel:[0,0,1]
	v_pk_mul_f32 v[10:11], v[68:69], s[12:13] op_sel_hi:[1,0]
	v_pk_mul_f32 v[14:15], v[60:61], s[12:13] op_sel_hi:[1,0]
	v_med3_f32 v10, v10, s52, v175
	global_store_dwordx2 v[222:223], v[12:13], off offset:1536
	v_pk_mul_f32 v[12:13], v[66:67], s[12:13] op_sel_hi:[1,0]
	v_med3_f32 v11, v11, s52, v175
	v_med3_f32 v18, v12, s52, v175
	v_med3_f32 v13, v13, s52, v175
	v_cvt_pk_fp8_f32 v12, v18, v13
	v_mov_b32_e32 v13, 0
	v_lshl_add_u64 v[8:9], v[6:7], 0, s[22:23]
	v_cvt_pk_fp8_f32 v12, v10, v11 op_sel:[0,0,1]
	v_med3_f32 v10, v16, s52, v175
	v_med3_f32 v11, v17, s52, v175
	v_cvt_pk_fp8_f32 v13, v10, v11
	v_med3_f32 v10, v14, s52, v175
	v_med3_f32 v11, v15, s52, v175
	v_pk_mul_f32 v[16:17], v[46:47], s[12:13] op_sel_hi:[1,0]
	v_cvt_pk_fp8_f32 v13, v10, v11 op_sel:[0,0,1]
	v_add_co_u32_e32 v10, vcc, s65, v6
	v_pk_mul_f32 v[14:15], v[48:49], s[12:13] op_sel_hi:[1,0]
	s_nop 0
	v_addc_co_u32_e32 v11, vcc, 0, v7, vcc
	global_store_dwordx2 v[222:223], v[12:13], off offset:2048
	v_pk_mul_f32 v[12:13], v[54:55], s[12:13] op_sel_hi:[1,0]
	v_pk_mul_f32 v[10:11], v[56:57], s[12:13] op_sel_hi:[1,0]
	v_med3_f32 v18, v12, s52, v175
	v_med3_f32 v13, v13, s52, v175
	v_cvt_pk_fp8_f32 v12, v18, v13
	v_med3_f32 v10, v10, s52, v175
	v_med3_f32 v11, v11, s52, v175
	v_cvt_pk_fp8_f32 v12, v10, v11 op_sel:[0,0,1]
	v_med3_f32 v10, v16, s52, v175
	v_med3_f32 v11, v17, s52, v175
	v_cvt_pk_fp8_f32 v13, v10, v11
	v_med3_f32 v10, v14, s52, v175
	v_med3_f32 v11, v15, s52, v175
	v_pk_mul_f32 v[16:17], v[42:43], s[12:13] op_sel_hi:[1,0]
	v_cvt_pk_fp8_f32 v13, v10, v11 op_sel:[0,0,1]
	v_pk_mul_f32 v[10:11], v[52:53], s[12:13] op_sel_hi:[1,0]
	v_pk_mul_f32 v[14:15], v[44:45], s[12:13] op_sel_hi:[1,0]
	v_med3_f32 v10, v10, s52, v175
	global_store_dwordx2 v[222:223], v[12:13], off offset:2560
	v_pk_mul_f32 v[12:13], v[50:51], s[12:13] op_sel_hi:[1,0]
	v_med3_f32 v11, v11, s52, v175
	v_med3_f32 v18, v12, s52, v175
	v_med3_f32 v13, v13, s52, v175
	v_cvt_pk_fp8_f32 v12, v18, v13
	v_lshl_add_u64 v[8:9], v[6:7], 0, s[40:41]
	v_add_co_u32_e32 v6, vcc, s30, v6
	v_cvt_pk_fp8_f32 v12, v10, v11 op_sel:[0,0,1]
	v_med3_f32 v10, v16, s52, v175
	v_med3_f32 v11, v17, s52, v175
	v_cvt_pk_fp8_f32 v13, v10, v11
	v_med3_f32 v10, v14, s52, v175
	v_med3_f32 v11, v15, s52, v175
	v_addc_co_u32_e32 v7, vcc, 0, v7, vcc
	v_cvt_pk_fp8_f32 v13, v10, v11 op_sel:[0,0,1]
	v_pk_mul_f32 v[10:11], v[38:39], s[12:13] op_sel_hi:[1,0]
	v_pk_mul_f32 v[14:15], v[34:35], s[12:13] op_sel_hi:[1,0]
	v_med3_f32 v16, v10, s52, v175
	v_med3_f32 v11, v11, s52, v175
	v_cvt_pk_fp8_f32 v10, v16, v11
	global_store_dwordx2 v[222:223], v[12:13], off offset:3072
	v_pk_mul_f32 v[6:7], v[40:41], s[12:13] op_sel_hi:[1,0]
	v_mov_b32_e32 v11, 0
	v_med3_f32 v6, v6, s52, v175
	v_med3_f32 v7, v7, s52, v175
	v_cvt_pk_fp8_f32 v10, v6, v7 op_sel:[0,0,1]
	v_med3_f32 v6, v14, s52, v175
	v_med3_f32 v7, v15, s52, v175
	v_cvt_pk_fp8_f32 v11, v6, v7
	v_pk_mul_f32 v[12:13], v[36:37], s[12:13] op_sel_hi:[1,0]
	s_nop 0
	v_med3_f32 v6, v12, s52, v175
	v_med3_f32 v7, v13, s52, v175
	v_cvt_pk_fp8_f32 v11, v6, v7 op_sel:[0,0,1]
	global_store_dwordx2 v[222:223], v[10:11], off offset:3584
	s_cbranch_execnz .LBB0_222

.LBB0_2094:
.LBB0_2096:
	v_mov_b32_e32 v2, v166
	v_mov_b32_e32 v3, v165
	v_mov_b32_e32 v4, s39
	ds_read_b32 v4, v4 offset:288
	s_lshl_b32 s15, s85, 11
	v_lshlrev_b32_e32 v18, 3, v2
	s_add_i32 s15, s15, 0
	s_add_i32 s15, s15, 0x21000
	v_add_u32_e32 v2, s66, v18
	v_lshl_add_u32 v8, v2, 2, s15
	ds_read_b128 v[10:13], v8
	s_waitcnt lgkmcnt(1)
	v_readfirstlane_b32 s17, v4
	s_lshl_b32 s17, s17, 2
	s_add_i32 s17, s17, 0
	s_add_i32 s17, s17, 0x201c0
	v_mov_b32_e32 v2, s17
	ds_read2_b32 v[6:7], v2 offset1:32
	v_add_u32_e32 v19, s29, v3
	v_add_u32_e32 v21, 16, v19
	v_add_u32_e32 v23, 32, v19
	v_lshl_add_u32 v22, v21, 2, s15
	s_waitcnt lgkmcnt(0)
	v_readfirstlane_b32 s17, v7
	s_sub_i32 s17, s22, s17
	v_readfirstlane_b32 s26, v6
	v_lshl_add_u32 v6, v19, 2, s15
	v_lshl_add_u32 v24, v23, 2, s15
	ds_read_b128 v[14:17], v8 offset:16
	ds_read_b128 v[2:5], v8 offset:512
	s_lshl_b32 s17, s17, 8
	ds_read_b32 v25, v6 offset:1024
	ds_read_b128 v[6:9], v8 offset:528
	ds_read_b32 v22, v22 offset:1024
	ds_read_b32 v24, v24 offset:1024
	v_add_u32_e32 v20, s17, v19
	v_cmp_gt_i32_e32 vcc, s26, v20
	v_add_u32_e32 v20, s17, v21
	v_add_u32_e32 v27, 0xa0, v19
	s_waitcnt lgkmcnt(3)
	v_cndmask_b32_e32 v176, 0, v25, vcc
	v_cmp_gt_i32_e32 vcc, s26, v20
	v_add_u32_e32 v20, s17, v23
	v_add_u32_e32 v29, 0xb0, v19
	s_waitcnt lgkmcnt(1)
	v_cndmask_b32_e32 v178, 0, v22, vcc
	v_cmp_gt_i32_e32 vcc, s26, v20
	v_add_u32_e32 v20, 48, v19
	v_add_u32_e32 v22, 0x80, v19
	s_waitcnt lgkmcnt(0)
	v_cndmask_b32_e32 v32, 0, v24, vcc
	v_add_u32_e32 v24, 0x90, v19
	v_lshl_add_u32 v21, v20, 2, s15
	v_add_u32_e32 v20, s17, v20
	v_lshl_add_u32 v23, v22, 2, s15
	v_lshl_add_u32 v25, v24, 2, s15
	v_lshl_add_u32 v26, v27, 2, s15
	v_lshl_add_u32 v28, v29, 2, s15
	ds_read_b32 v21, v21 offset:1024
	ds_read_b32 v23, v23 offset:1024
	ds_read_b32 v25, v25 offset:1024
	ds_read_b32 v31, v26 offset:1024
	ds_read_b32 v33, v28 offset:1024
	v_cmp_gt_i32_e32 vcc, s26, v20
	v_add_u32_e32 v20, s17, v22
	v_mul_f32_e32 v180, 0x3b800000, v176
	s_waitcnt lgkmcnt(4)
	v_cndmask_b32_e32 v30, 0, v21, vcc
	v_cmp_gt_i32_e32 vcc, s26, v20
	v_lshl_add_u32 v22, s22, 8, v19
	v_pk_mul_f32 v[158:159], v[158:159], v[180:181] op_sel_hi:[1,0]
	s_waitcnt lgkmcnt(3)
	v_cndmask_b32_e32 v28, 0, v23, vcc
	v_add_u32_e32 v20, s17, v24
	v_ashrrev_i32_e32 v23, 31, v22
	v_pk_fma_f32 v[158:159], v[10:11], v[176:177], v[158:159] op_sel_hi:[1,0,1]
	v_pk_mul_f32 v[154:155], v[154:155], v[180:181] op_sel_hi:[1,0]
	v_cmp_gt_i32_e32 vcc, s26, v20
	v_lshlrev_b64 v[182:183], 10, v[22:23]
	v_pk_fma_f32 v[154:155], v[14:15], v[176:177], v[154:155] op_sel_hi:[1,0,1]
	v_med3_f32 v21, v158, s83, v173
	v_med3_f32 v23, v159, s83, v173
	s_waitcnt lgkmcnt(2)
	v_cndmask_b32_e32 v26, 0, v25, vcc
	v_add_u32_e32 v20, s17, v27
	v_cvt_pk_fp8_f32 v158, v21, v23
	v_med3_f32 v25, v154, s83, v173
	v_med3_f32 v27, v155, s83, v173
	v_pk_mul_f32 v[160:161], v[160:161], v[180:181] op_sel_hi:[1,0]
	v_cvt_pk_fp8_f32 v159, v25, v27
	v_pk_fma_f32 v[160:161], v[12:13], v[176:177], v[160:161] op_sel_hi:[1,0,1]
	v_pk_mul_f32 v[156:157], v[156:157], v[180:181] op_sel_hi:[1,0]
	v_med3_f32 v21, v160, s83, v173
	v_pk_fma_f32 v[156:157], v[16:17], v[176:177], v[156:157] op_sel_hi:[1,0,1]
	v_med3_f32 v23, v161, s83, v173
	v_pk_mul_f32 v[150:151], v[150:151], v[180:181] op_sel_hi:[1,0]
	v_cvt_pk_fp8_f32 v158, v21, v23 op_sel:[0,0,1]
	v_med3_f32 v21, v156, s83, v173
	v_med3_f32 v23, v157, s83, v173
	v_pk_fma_f32 v[150:151], v[2:3], v[176:177], v[150:151] op_sel_hi:[1,0,1]
	v_pk_mul_f32 v[146:147], v[146:147], v[180:181] op_sel_hi:[1,0]
	v_cvt_pk_fp8_f32 v159, v21, v23 op_sel:[0,0,1]
	v_pk_fma_f32 v[146:147], v[6:7], v[176:177], v[146:147] op_sel_hi:[1,0,1]
	v_med3_f32 v21, v150, s83, v173
	v_med3_f32 v23, v151, s83, v173
	v_cvt_pk_fp8_f32 v150, v21, v23
	v_med3_f32 v25, v146, s83, v173
	v_med3_f32 v27, v147, s83, v173
	v_pk_mul_f32 v[152:153], v[152:153], v[180:181] op_sel_hi:[1,0]
	v_cvt_pk_fp8_f32 v151, v25, v27
	v_pk_fma_f32 v[152:153], v[4:5], v[176:177], v[152:153] op_sel_hi:[1,0,1]
	v_pk_mul_f32 v[148:149], v[148:149], v[180:181] op_sel_hi:[1,0]
	v_med3_f32 v21, v152, s83, v173
	v_pk_fma_f32 v[148:149], v[8:9], v[176:177], v[148:149] op_sel_hi:[1,0,1]
	v_med3_f32 v23, v153, s83, v173
	s_or_b32 s27, s38, s66
	v_cvt_pk_fp8_f32 v150, v21, v23 op_sel:[0,0,1]
	v_med3_f32 v21, v148, s83, v173
	v_med3_f32 v23, v149, s83, v173
	v_add_u32_e32 v18, s27, v18
	v_cvt_pk_fp8_f32 v151, v21, v23 op_sel:[0,0,1]
	v_ashrrev_i32_e32 v19, 31, v18
	v_lshl_add_u64 v[146:147], s[10:11], 0, v[182:183]
	v_lshl_add_u64 v[146:147], v[146:147], 0, v[18:19]
	global_store_dwordx2 v[146:147], v[158:159], off
	global_store_dwordx2 v[146:147], v[150:151], off offset:128
	v_mul_f32_e32 v146, 0x3b800000, v178
	v_pk_mul_f32 v[142:143], v[142:143], v[146:147] op_sel_hi:[1,0]
	v_pk_mul_f32 v[138:139], v[138:139], v[146:147] op_sel_hi:[1,0]
	v_pk_fma_f32 v[142:143], v[10:11], v[178:179], v[142:143] op_sel_hi:[1,0,1]
	v_pk_fma_f32 v[138:139], v[14:15], v[178:179], v[138:139] op_sel_hi:[1,0,1]
	v_med3_f32 v21, v142, s83, v173
	v_med3_f32 v23, v143, s83, v173
	v_cvt_pk_fp8_f32 v142, v21, v23
	v_med3_f32 v25, v138, s83, v173
	v_med3_f32 v27, v139, s83, v173
	v_pk_mul_f32 v[144:145], v[144:145], v[146:147] op_sel_hi:[1,0]
	v_cvt_pk_fp8_f32 v143, v25, v27
	v_pk_fma_f32 v[144:145], v[12:13], v[178:179], v[144:145] op_sel_hi:[1,0,1]
	v_pk_mul_f32 v[140:141], v[140:141], v[146:147] op_sel_hi:[1,0]
	v_med3_f32 v21, v144, s83, v173
	v_pk_fma_f32 v[140:141], v[16:17], v[178:179], v[140:141] op_sel_hi:[1,0,1]
	v_med3_f32 v23, v145, s83, v173
	v_pk_mul_f32 v[134:135], v[134:135], v[146:147] op_sel_hi:[1,0]
	v_cvt_pk_fp8_f32 v142, v21, v23 op_sel:[0,0,1]
	v_med3_f32 v21, v140, s83, v173
	v_med3_f32 v23, v141, s83, v173
	v_pk_fma_f32 v[134:135], v[2:3], v[178:179], v[134:135] op_sel_hi:[1,0,1]
	v_pk_mul_f32 v[130:131], v[130:131], v[146:147] op_sel_hi:[1,0]
	v_cvt_pk_fp8_f32 v143, v21, v23 op_sel:[0,0,1]
	v_pk_fma_f32 v[130:131], v[6:7], v[178:179], v[130:131] op_sel_hi:[1,0,1]
	v_med3_f32 v21, v134, s83, v173
	v_med3_f32 v23, v135, s83, v173
	v_cvt_pk_fp8_f32 v134, v21, v23
	v_med3_f32 v25, v130, s83, v173
	v_med3_f32 v27, v131, s83, v173
	v_pk_mul_f32 v[136:137], v[136:137], v[146:147] op_sel_hi:[1,0]
	v_cvt_pk_fp8_f32 v135, v25, v27
	v_pk_fma_f32 v[136:137], v[4:5], v[178:179], v[136:137] op_sel_hi:[1,0,1]
	v_pk_mul_f32 v[132:133], v[132:133], v[146:147] op_sel_hi:[1,0]
	v_add_u32_e32 v148, 16, v22
	v_pk_fma_f32 v[132:133], v[8:9], v[178:179], v[132:133] op_sel_hi:[1,0,1]
	v_med3_f32 v21, v136, s83, v173
	v_med3_f32 v23, v137, s83, v173
	v_ashrrev_i32_e32 v149, 31, v148
	v_cvt_pk_fp8_f32 v134, v21, v23 op_sel:[0,0,1]
	v_med3_f32 v21, v132, s83, v173
	v_med3_f32 v23, v133, s83, v173
	v_lshlrev_b64 v[148:149], 10, v[148:149]
	v_cvt_pk_fp8_f32 v135, v21, v23 op_sel:[0,0,1]
	v_lshl_add_u64 v[130:131], s[10:11], 0, v[148:149]
	v_lshl_add_u64 v[130:131], v[130:131], 0, v[18:19]
	global_store_dwordx2 v[130:131], v[142:143], off
	global_store_dwordx2 v[130:131], v[134:135], off offset:128
	v_mul_f32_e32 v130, 0x3b800000, v32
	v_pk_mul_f32 v[126:127], v[126:127], v[130:131] op_sel_hi:[1,0]
	v_pk_mul_f32 v[122:123], v[122:123], v[130:131] op_sel_hi:[1,0]
	s_waitcnt lgkmcnt(0)
	v_pk_fma_f32 v[126:127], v[10:11], v[32:33], v[126:127] op_sel_hi:[1,0,1]
	v_pk_fma_f32 v[122:123], v[14:15], v[32:33], v[122:123] op_sel_hi:[1,0,1]
	v_med3_f32 v21, v126, s83, v173
	v_med3_f32 v23, v127, s83, v173
	v_cvt_pk_fp8_f32 v126, v21, v23
	v_med3_f32 v25, v122, s83, v173
	v_med3_f32 v27, v123, s83, v173
	v_pk_mul_f32 v[128:129], v[128:129], v[130:131] op_sel_hi:[1,0]
	v_cvt_pk_fp8_f32 v127, v25, v27
	v_pk_fma_f32 v[128:129], v[12:13], v[32:33], v[128:129] op_sel_hi:[1,0,1]
	v_pk_mul_f32 v[124:125], v[124:125], v[130:131] op_sel_hi:[1,0]
	v_cmp_gt_i32_e32 vcc, s26, v20
	v_add_u32_e32 v20, s17, v29
	v_pk_fma_f32 v[124:125], v[16:17], v[32:33], v[124:125] op_sel_hi:[1,0,1]
	v_med3_f32 v21, v128, s83, v173
	v_med3_f32 v23, v129, s83, v173
	v_pk_mul_f32 v[118:119], v[118:119], v[130:131] op_sel_hi:[1,0]
	v_cndmask_b32_e32 v24, 0, v31, vcc
	v_cmp_gt_i32_e32 vcc, s26, v20
	v_cvt_pk_fp8_f32 v126, v21, v23 op_sel:[0,0,1]
	v_med3_f32 v21, v124, s83, v173
	v_med3_f32 v23, v125, s83, v173
	v_pk_mul_f32 v[120:121], v[120:121], v[130:131] op_sel_hi:[1,0]
	v_pk_fma_f32 v[118:119], v[2:3], v[32:33], v[118:119] op_sel_hi:[1,0,1]
	v_pk_mul_f32 v[114:115], v[114:115], v[130:131] op_sel_hi:[1,0]
	v_pk_mul_f32 v[116:117], v[116:117], v[130:131] op_sel_hi:[1,0]
	v_cndmask_b32_e32 v20, 0, v33, vcc
	v_cvt_pk_fp8_f32 v127, v21, v23 op_sel:[0,0,1]
	v_pk_fma_f32 v[120:121], v[4:5], v[32:33], v[120:121] op_sel_hi:[1,0,1]
	v_pk_fma_f32 v[116:117], v[8:9], v[32:33], v[116:117] op_sel_hi:[1,0,1]
	v_pk_fma_f32 v[32:33], v[6:7], v[32:33], v[114:115] op_sel_hi:[1,0,1]
	v_med3_f32 v21, v118, s83, v173
	v_med3_f32 v23, v119, s83, v173
	v_cvt_pk_fp8_f32 v114, v21, v23
	v_med3_f32 v25, v32, s83, v173
	v_med3_f32 v27, v33, s83, v173
	v_cvt_pk_fp8_f32 v115, v25, v27
	v_add_u32_e32 v132, 32, v22
	v_med3_f32 v21, v120, s83, v173
	v_med3_f32 v23, v121, s83, v173
	v_ashrrev_i32_e32 v133, 31, v132
	v_cvt_pk_fp8_f32 v114, v21, v23 op_sel:[0,0,1]
	v_med3_f32 v21, v116, s83, v173
	v_med3_f32 v23, v117, s83, v173
	v_lshlrev_b64 v[132:133], 10, v[132:133]
	v_cvt_pk_fp8_f32 v115, v21, v23 op_sel:[0,0,1]
	v_lshl_add_u64 v[32:33], s[10:11], 0, v[132:133]
	v_lshl_add_u64 v[32:33], v[32:33], 0, v[18:19]
	global_store_dwordx2 v[32:33], v[126:127], off
	global_store_dwordx2 v[32:33], v[114:115], off offset:128
	v_mul_f32_e32 v32, 0x3b800000, v30
	v_pk_mul_f32 v[110:111], v[110:111], v[32:33] op_sel_hi:[1,0]
	v_pk_mul_f32 v[106:107], v[106:107], v[32:33] op_sel_hi:[1,0]
	v_pk_fma_f32 v[110:111], v[10:11], v[30:31], v[110:111] op_sel_hi:[1,0,1]
	v_pk_fma_f32 v[106:107], v[14:15], v[30:31], v[106:107] op_sel_hi:[1,0,1]
	v_med3_f32 v21, v110, s83, v173
	v_med3_f32 v23, v111, s83, v173
	v_cvt_pk_fp8_f32 v110, v21, v23
	v_med3_f32 v25, v106, s83, v173
	v_med3_f32 v27, v107, s83, v173
	v_pk_mul_f32 v[112:113], v[112:113], v[32:33] op_sel_hi:[1,0]
	v_cvt_pk_fp8_f32 v111, v25, v27
	v_pk_fma_f32 v[112:113], v[12:13], v[30:31], v[112:113] op_sel_hi:[1,0,1]
	v_pk_mul_f32 v[108:109], v[108:109], v[32:33] op_sel_hi:[1,0]
	v_med3_f32 v21, v112, s83, v173
	v_pk_fma_f32 v[108:109], v[16:17], v[30:31], v[108:109] op_sel_hi:[1,0,1]
	v_med3_f32 v23, v113, s83, v173
	v_pk_mul_f32 v[102:103], v[102:103], v[32:33] op_sel_hi:[1,0]
	v_cvt_pk_fp8_f32 v110, v21, v23 op_sel:[0,0,1]
	v_med3_f32 v21, v108, s83, v173
	v_med3_f32 v23, v109, s83, v173
	v_pk_mul_f32 v[104:105], v[104:105], v[32:33] op_sel_hi:[1,0]
	v_pk_fma_f32 v[102:103], v[2:3], v[30:31], v[102:103] op_sel_hi:[1,0,1]
	v_pk_mul_f32 v[98:99], v[98:99], v[32:33] op_sel_hi:[1,0]
	v_pk_mul_f32 v[32:33], v[100:101], v[32:33] op_sel_hi:[1,0]
	v_cvt_pk_fp8_f32 v111, v21, v23 op_sel:[0,0,1]
	v_pk_fma_f32 v[104:105], v[4:5], v[30:31], v[104:105] op_sel_hi:[1,0,1]
	v_pk_fma_f32 v[32:33], v[8:9], v[30:31], v[32:33] op_sel_hi:[1,0,1]
	v_pk_fma_f32 v[30:31], v[6:7], v[30:31], v[98:99] op_sel_hi:[1,0,1]
	v_med3_f32 v21, v102, s83, v173
	v_med3_f32 v23, v103, s83, v173
	v_cvt_pk_fp8_f32 v98, v21, v23
	v_med3_f32 v25, v30, s83, v173
	v_med3_f32 v27, v31, s83, v173
	v_med3_f32 v21, v104, s83, v173
	v_med3_f32 v23, v105, s83, v173
	v_cvt_pk_fp8_f32 v99, v25, v27
	v_cvt_pk_fp8_f32 v98, v21, v23 op_sel:[0,0,1]
	v_med3_f32 v21, v32, s83, v173
	v_mul_f32_e32 v32, 0x3b800000, v28
	v_pk_mul_f32 v[94:95], v[94:95], v[32:33] op_sel_hi:[1,0]
	v_med3_f32 v23, v33, s83, v173
	v_pk_fma_f32 v[94:95], v[10:11], v[28:29], v[94:95] op_sel_hi:[1,0,1]
	v_pk_mul_f32 v[90:91], v[90:91], v[32:33] op_sel_hi:[1,0]
	v_cvt_pk_fp8_f32 v99, v21, v23 op_sel:[0,0,1]
	v_pk_fma_f32 v[90:91], v[14:15], v[28:29], v[90:91] op_sel_hi:[1,0,1]
	v_med3_f32 v21, v94, s83, v173
	v_med3_f32 v23, v95, s83, v173
	v_cvt_pk_fp8_f32 v94, v21, v23
	v_med3_f32 v25, v90, s83, v173
	v_med3_f32 v27, v91, s83, v173
	v_pk_mul_f32 v[96:97], v[96:97], v[32:33] op_sel_hi:[1,0]
	v_cvt_pk_fp8_f32 v95, v25, v27
	v_pk_fma_f32 v[96:97], v[12:13], v[28:29], v[96:97] op_sel_hi:[1,0,1]
	v_pk_mul_f32 v[92:93], v[92:93], v[32:33] op_sel_hi:[1,0]
	v_med3_f32 v21, v96, s83, v173
	v_pk_fma_f32 v[92:93], v[16:17], v[28:29], v[92:93] op_sel_hi:[1,0,1]
	v_med3_f32 v23, v97, s83, v173
	v_pk_mul_f32 v[86:87], v[86:87], v[32:33] op_sel_hi:[1,0]
	v_add_u32_e32 v114, 48, v22
	v_cvt_pk_fp8_f32 v94, v21, v23 op_sel:[0,0,1]
	v_med3_f32 v21, v92, s83, v173
	v_med3_f32 v23, v93, s83, v173
	v_pk_mul_f32 v[88:89], v[88:89], v[32:33] op_sel_hi:[1,0]
	v_pk_fma_f32 v[86:87], v[2:3], v[28:29], v[86:87] op_sel_hi:[1,0,1]
	v_pk_mul_f32 v[82:83], v[82:83], v[32:33] op_sel_hi:[1,0]
	v_pk_mul_f32 v[32:33], v[84:85], v[32:33] op_sel_hi:[1,0]
	v_ashrrev_i32_e32 v115, 31, v114
	v_cvt_pk_fp8_f32 v95, v21, v23 op_sel:[0,0,1]
	v_pk_fma_f32 v[88:89], v[4:5], v[28:29], v[88:89] op_sel_hi:[1,0,1]
	v_pk_fma_f32 v[32:33], v[8:9], v[28:29], v[32:33] op_sel_hi:[1,0,1]
	v_pk_fma_f32 v[28:29], v[6:7], v[28:29], v[82:83] op_sel_hi:[1,0,1]
	v_med3_f32 v21, v86, s83, v173
	v_med3_f32 v23, v87, s83, v173
	v_lshlrev_b64 v[114:115], 10, v[114:115]
	v_cvt_pk_fp8_f32 v82, v21, v23
	v_med3_f32 v25, v28, s83, v173
	v_med3_f32 v27, v29, s83, v173
	v_lshl_add_u64 v[30:31], s[10:11], 0, v[114:115]
	v_cvt_pk_fp8_f32 v83, v25, v27
	v_lshl_add_u64 v[30:31], v[30:31], 0, v[18:19]
	global_store_dwordx2 v[30:31], v[110:111], off
	global_store_dwordx2 v[30:31], v[98:99], off offset:128
	v_add_u32_e32 v30, 0x80, v22
	v_med3_f32 v21, v88, s83, v173
	v_med3_f32 v23, v89, s83, v173
	v_ashrrev_i32_e32 v31, 31, v30
	v_cvt_pk_fp8_f32 v82, v21, v23 op_sel:[0,0,1]
	v_med3_f32 v21, v32, s83, v173
	v_med3_f32 v23, v33, s83, v173
	v_lshlrev_b64 v[30:31], 10, v[30:31]
	v_cvt_pk_fp8_f32 v83, v21, v23 op_sel:[0,0,1]
	v_lshl_add_u64 v[28:29], s[10:11], 0, v[30:31]
	v_lshl_add_u64 v[28:29], v[28:29], 0, v[18:19]
	global_store_dwordx2 v[28:29], v[94:95], off
	global_store_dwordx2 v[28:29], v[82:83], off offset:128
	v_mul_f32_e32 v28, 0x3b800000, v26
	v_pk_mul_f32 v[32:33], v[78:79], v[28:29] op_sel_hi:[1,0]
	v_pk_mul_f32 v[74:75], v[74:75], v[28:29] op_sel_hi:[1,0]
	v_pk_fma_f32 v[32:33], v[10:11], v[26:27], v[32:33] op_sel_hi:[1,0,1]
	v_pk_mul_f32 v[78:79], v[80:81], v[28:29] op_sel_hi:[1,0]
	v_pk_mul_f32 v[76:77], v[76:77], v[28:29] op_sel_hi:[1,0]
	v_pk_fma_f32 v[74:75], v[14:15], v[26:27], v[74:75] op_sel_hi:[1,0,1]
	v_med3_f32 v21, v32, s83, v173
	v_med3_f32 v23, v33, s83, v173
	v_pk_fma_f32 v[78:79], v[12:13], v[26:27], v[78:79] op_sel_hi:[1,0,1]
	v_pk_fma_f32 v[76:77], v[16:17], v[26:27], v[76:77] op_sel_hi:[1,0,1]
	v_cvt_pk_fp8_f32 v32, v21, v23
	v_med3_f32 v25, v74, s83, v173
	v_med3_f32 v27, v75, s83, v173
	v_cvt_pk_fp8_f32 v33, v25, v27
	v_med3_f32 v21, v78, s83, v173
	v_med3_f32 v23, v79, s83, v173
	v_pk_mul_f32 v[70:71], v[70:71], v[28:29] op_sel_hi:[1,0]
	v_cvt_pk_fp8_f32 v32, v21, v23 op_sel:[0,0,1]
	v_med3_f32 v21, v76, s83, v173
	v_med3_f32 v23, v77, s83, v173
	v_pk_mul_f32 v[72:73], v[72:73], v[28:29] op_sel_hi:[1,0]
	v_pk_fma_f32 v[70:71], v[2:3], v[26:27], v[70:71] op_sel_hi:[1,0,1]
	v_pk_mul_f32 v[66:67], v[66:67], v[28:29] op_sel_hi:[1,0]
	v_pk_mul_f32 v[28:29], v[68:69], v[28:29] op_sel_hi:[1,0]
	v_cvt_pk_fp8_f32 v33, v21, v23 op_sel:[0,0,1]
	v_pk_fma_f32 v[72:73], v[4:5], v[26:27], v[72:73] op_sel_hi:[1,0,1]
	v_pk_fma_f32 v[28:29], v[8:9], v[26:27], v[28:29] op_sel_hi:[1,0,1]
	v_pk_fma_f32 v[26:27], v[6:7], v[26:27], v[66:67] op_sel_hi:[1,0,1]
	v_med3_f32 v21, v70, s83, v173
	v_med3_f32 v23, v71, s83, v173
	v_cvt_pk_fp8_f32 v66, v21, v23
	v_med3_f32 v25, v26, s83, v173
	v_med3_f32 v26, v27, s83, v173
	v_cvt_pk_fp8_f32 v67, v25, v26
	v_add_u32_e32 v30, 0x90, v22
	v_med3_f32 v21, v72, s83, v173
	v_med3_f32 v23, v73, s83, v173
	v_ashrrev_i32_e32 v31, 31, v30
	v_cvt_pk_fp8_f32 v66, v21, v23 op_sel:[0,0,1]
	v_med3_f32 v21, v28, s83, v173
	v_med3_f32 v23, v29, s83, v173
	v_lshlrev_b64 v[30:31], 10, v[30:31]
	v_cvt_pk_fp8_f32 v67, v21, v23 op_sel:[0,0,1]
	v_lshl_add_u64 v[26:27], s[10:11], 0, v[30:31]
	v_lshl_add_u64 v[26:27], v[26:27], 0, v[18:19]
	global_store_dwordx2 v[26:27], v[32:33], off
	global_store_dwordx2 v[26:27], v[66:67], off offset:128
	v_mul_f32_e32 v26, 0x3b800000, v24
	v_pk_mul_f32 v[30:31], v[62:63], v[26:27] op_sel_hi:[1,0]
	v_pk_mul_f32 v[58:59], v[58:59], v[26:27] op_sel_hi:[1,0]
	v_pk_fma_f32 v[30:31], v[10:11], v[24:25], v[30:31] op_sel_hi:[1,0,1]
	v_pk_mul_f32 v[32:33], v[64:65], v[26:27] op_sel_hi:[1,0]
	v_pk_mul_f32 v[60:61], v[60:61], v[26:27] op_sel_hi:[1,0]
	v_pk_fma_f32 v[58:59], v[14:15], v[24:25], v[58:59] op_sel_hi:[1,0,1]
	v_med3_f32 v21, v30, s83, v173
	v_med3_f32 v23, v31, s83, v173
	v_pk_fma_f32 v[32:33], v[12:13], v[24:25], v[32:33] op_sel_hi:[1,0,1]
	v_pk_fma_f32 v[60:61], v[16:17], v[24:25], v[60:61] op_sel_hi:[1,0,1]
	v_cvt_pk_fp8_f32 v30, v21, v23
	v_med3_f32 v25, v58, s83, v173
	v_med3_f32 v27, v59, s83, v173
	v_cvt_pk_fp8_f32 v31, v25, v27
	v_med3_f32 v21, v32, s83, v173
	v_med3_f32 v23, v33, s83, v173
	v_pk_mul_f32 v[32:33], v[54:55], v[26:27] op_sel_hi:[1,0]
	v_cvt_pk_fp8_f32 v30, v21, v23 op_sel:[0,0,1]
	v_med3_f32 v21, v60, s83, v173
	v_med3_f32 v23, v61, s83, v173
	v_pk_mul_f32 v[54:55], v[56:57], v[26:27] op_sel_hi:[1,0]
	v_pk_fma_f32 v[32:33], v[2:3], v[24:25], v[32:33] op_sel_hi:[1,0,1]
	v_pk_mul_f32 v[50:51], v[50:51], v[26:27] op_sel_hi:[1,0]
	v_pk_mul_f32 v[26:27], v[52:53], v[26:27] op_sel_hi:[1,0]
	v_cvt_pk_fp8_f32 v31, v21, v23 op_sel:[0,0,1]
	v_pk_fma_f32 v[54:55], v[4:5], v[24:25], v[54:55] op_sel_hi:[1,0,1]
	v_pk_fma_f32 v[26:27], v[8:9], v[24:25], v[26:27] op_sel_hi:[1,0,1]
	v_pk_fma_f32 v[24:25], v[6:7], v[24:25], v[50:51] op_sel_hi:[1,0,1]
	v_med3_f32 v21, v32, s83, v173
	v_med3_f32 v23, v33, s83, v173
	v_cvt_pk_fp8_f32 v32, v21, v23
	v_med3_f32 v24, v24, s83, v173
	v_med3_f32 v25, v25, s83, v173
	v_cvt_pk_fp8_f32 v33, v24, v25
	v_add_u32_e32 v28, 0xa0, v22
	v_med3_f32 v21, v54, s83, v173
	v_med3_f32 v23, v55, s83, v173
	v_ashrrev_i32_e32 v29, 31, v28
	v_cvt_pk_fp8_f32 v32, v21, v23 op_sel:[0,0,1]
	v_med3_f32 v21, v26, s83, v173
	v_med3_f32 v23, v27, s83, v173
	v_lshlrev_b64 v[28:29], 10, v[28:29]
	v_cvt_pk_fp8_f32 v33, v21, v23 op_sel:[0,0,1]
	v_lshl_add_u64 v[24:25], s[10:11], 0, v[28:29]
	v_lshl_add_u64 v[24:25], v[24:25], 0, v[18:19]
	global_store_dwordx2 v[24:25], v[30:31], off
	global_store_dwordx2 v[24:25], v[32:33], off offset:128
	v_mul_f32_e32 v24, 0x3b800000, v20
	v_pk_mul_f32 v[26:27], v[46:47], v[24:25] op_sel_hi:[1,0]
	v_pk_mul_f32 v[28:29], v[48:49], v[24:25] op_sel_hi:[1,0]
	v_pk_fma_f32 v[10:11], v[10:11], v[20:21], v[26:27] op_sel_hi:[1,0,1]
	v_pk_fma_f32 v[12:13], v[12:13], v[20:21], v[28:29] op_sel_hi:[1,0,1]
	v_pk_mul_f32 v[26:27], v[42:43], v[24:25] op_sel_hi:[1,0]
	v_pk_mul_f32 v[28:29], v[44:45], v[24:25] op_sel_hi:[1,0]
	v_pk_fma_f32 v[14:15], v[14:15], v[20:21], v[26:27] op_sel_hi:[1,0,1]
	v_pk_fma_f32 v[16:17], v[16:17], v[20:21], v[28:29] op_sel_hi:[1,0,1]
	v_med3_f32 v21, v10, s83, v173
	v_med3_f32 v11, v11, s83, v173
	v_cvt_pk_fp8_f32 v10, v21, v11
	v_med3_f32 v14, v14, s83, v173
	v_med3_f32 v15, v15, s83, v173
	v_cvt_pk_fp8_f32 v11, v14, v15
	v_med3_f32 v12, v12, s83, v173
	v_med3_f32 v13, v13, s83, v173
	v_cvt_pk_fp8_f32 v10, v12, v13 op_sel:[0,0,1]
	v_med3_f32 v12, v16, s83, v173
	v_med3_f32 v13, v17, s83, v173
	v_cvt_pk_fp8_f32 v11, v12, v13 op_sel:[0,0,1]
	v_pk_mul_f32 v[12:13], v[38:39], v[24:25] op_sel_hi:[1,0]
	v_pk_mul_f32 v[14:15], v[40:41], v[24:25] op_sel_hi:[1,0]
	v_pk_fma_f32 v[2:3], v[2:3], v[20:21], v[12:13] op_sel_hi:[1,0,1]
	v_pk_mul_f32 v[12:13], v[34:35], v[24:25] op_sel_hi:[1,0]
	v_med3_f32 v3, v3, s83, v173
	v_pk_fma_f32 v[6:7], v[6:7], v[20:21], v[12:13] op_sel_hi:[1,0,1]
	v_med3_f32 v12, v2, s83, v173
	v_mov_b32_e32 v2, 0
	v_cvt_pk_fp8_f32 v2, v12, v3
	v_med3_f32 v6, v6, s83, v173
	v_med3_f32 v7, v7, s83, v173
	v_cvt_pk_fp8_f32 v3, v6, v7
	v_pk_fma_f32 v[4:5], v[4:5], v[20:21], v[14:15] op_sel_hi:[1,0,1]
	v_pk_mul_f32 v[14:15], v[36:37], v[24:25] op_sel_hi:[1,0]
	v_add_u32_e32 v22, 0xb0, v22
	v_pk_fma_f32 v[8:9], v[8:9], v[20:21], v[14:15] op_sel_hi:[1,0,1]
	v_med3_f32 v4, v4, s83, v173
	v_med3_f32 v5, v5, s83, v173
	v_ashrrev_i32_e32 v23, 31, v22
	v_cvt_pk_fp8_f32 v2, v4, v5 op_sel:[0,0,1]
	v_med3_f32 v4, v8, s83, v173
	v_med3_f32 v5, v9, s83, v173
	v_lshlrev_b64 v[22:23], 10, v[22:23]
	v_cvt_pk_fp8_f32 v3, v4, v5 op_sel:[0,0,1]
	v_lshl_add_u64 v[4:5], s[10:11], 0, v[22:23]
	v_lshl_add_u64 v[4:5], v[4:5], 0, v[18:19]
	s_and_b64 vcc, exec, s[6:7]
	s_mov_b64 s[6:7], -1
	v_readlane_b32 s90, v253, 26
	global_store_dwordx2 v[4:5], v[10:11], off
	global_store_dwordx2 v[4:5], v[2:3], off offset:128
	s_cbranch_vccnz .LBB0_2057
	s_andn2_b64 vcc, exec, s[8:9]
	s_cbranch_vccnz .LBB0_2056
	s_barrier
	s_branch .LBB0_2056

.LBB0_2132:
	s_nop 15
	s_nop 15
	v_mov_b32_e32 v0, v166
	v_mov_b32_e32 v1, v167
	v_mov_b32_e32 v2, s5
	ds_read_b32 v2, v2 offset:288
	s_lshl_b32 s5, s69, 11
	v_lshlrev_b32_e32 v16, 3, v1
	s_add_i32 s5, s5, 0
	s_add_i32 s5, s5, 0x21000
	v_add_u32_e32 v1, s53, v16
	v_lshl_add_u32 v6, v1, 2, s5
	ds_read_b128 v[8:11], v6
	s_waitcnt lgkmcnt(1)
	v_readfirstlane_b32 s13, v2
	s_lshl_b32 s13, s13, 2
	s_add_i32 s13, s13, 0
	s_add_i32 s13, s13, 0x201c0
	v_mov_b32_e32 v1, s13
	ds_read2_b32 v[4:5], v1 offset1:32
	v_add_u32_e32 v17, s52, v0
	v_add_u32_e32 v19, 16, v17
	v_add_u32_e32 v21, 32, v17
	v_lshl_add_u32 v20, v19, 2, s5
	s_waitcnt lgkmcnt(0)
	v_readfirstlane_b32 s13, v5
	s_sub_i32 s13, s20, s13
	v_readfirstlane_b32 s15, v4
	v_lshl_add_u32 v4, v17, 2, s5
	v_lshl_add_u32 v22, v21, 2, s5
	ds_read_b128 v[12:15], v6 offset:16
	ds_read_b128 v[0:3], v6 offset:512
	s_lshl_b32 s13, s13, 8
	ds_read_b32 v23, v4 offset:1024
	ds_read_b128 v[4:7], v6 offset:528
	ds_read_b32 v20, v20 offset:1024
	ds_read_b32 v22, v22 offset:1024
	v_add_u32_e32 v18, s13, v17
	v_cmp_gt_i32_e32 vcc, s15, v18
	v_add_u32_e32 v18, s13, v19
	v_add_u32_e32 v25, 0xa0, v17
	s_waitcnt lgkmcnt(3)
	v_cndmask_b32_e32 v172, 0, v23, vcc
	v_cmp_gt_i32_e32 vcc, s15, v18
	v_add_u32_e32 v18, s13, v21
	v_add_u32_e32 v27, 0xb0, v17
	s_waitcnt lgkmcnt(1)
	v_cndmask_b32_e32 v174, 0, v20, vcc
	v_cmp_gt_i32_e32 vcc, s15, v18
	v_add_u32_e32 v18, 48, v17
	v_add_u32_e32 v20, 0x80, v17
	s_waitcnt lgkmcnt(0)
	v_cndmask_b32_e32 v30, 0, v22, vcc
	v_add_u32_e32 v22, 0x90, v17
	v_lshl_add_u32 v19, v18, 2, s5
	v_add_u32_e32 v18, s13, v18
	v_lshl_add_u32 v21, v20, 2, s5
	v_lshl_add_u32 v23, v22, 2, s5
	v_lshl_add_u32 v24, v25, 2, s5
	v_lshl_add_u32 v26, v27, 2, s5
	ds_read_b32 v19, v19 offset:1024
	ds_read_b32 v21, v21 offset:1024
	ds_read_b32 v23, v23 offset:1024
	ds_read_b32 v29, v24 offset:1024
	ds_read_b32 v31, v26 offset:1024
	v_cmp_gt_i32_e32 vcc, s15, v18
	v_add_u32_e32 v18, s13, v20
	v_mul_f32_e32 v176, 0x3b800000, v172
	s_waitcnt lgkmcnt(4)
	v_cndmask_b32_e32 v28, 0, v19, vcc
	v_cmp_gt_i32_e32 vcc, s15, v18
	v_lshl_add_u32 v20, s20, 8, v17
	v_pk_mul_f32 v[156:157], v[156:157], v[176:177] op_sel_hi:[1,0]
	s_waitcnt lgkmcnt(3)
	v_cndmask_b32_e32 v26, 0, v21, vcc
	v_add_u32_e32 v18, s13, v22
	v_ashrrev_i32_e32 v21, 31, v20
	v_pk_fma_f32 v[156:157], v[8:9], v[172:173], v[156:157] op_sel_hi:[1,0,1]
	v_pk_mul_f32 v[152:153], v[152:153], v[176:177] op_sel_hi:[1,0]
	v_cmp_gt_i32_e32 vcc, s15, v18
	v_lshlrev_b64 v[178:179], 10, v[20:21]
	v_pk_fma_f32 v[152:153], v[12:13], v[172:173], v[152:153] op_sel_hi:[1,0,1]
	v_med3_f32 v19, v156, s67, v171
	v_med3_f32 v21, v157, s67, v171
	s_waitcnt lgkmcnt(2)
	v_cndmask_b32_e32 v24, 0, v23, vcc
	v_add_u32_e32 v18, s13, v25
	v_cvt_pk_fp8_f32 v156, v19, v21
	v_med3_f32 v23, v152, s67, v171
	v_med3_f32 v25, v153, s67, v171
	v_pk_mul_f32 v[158:159], v[158:159], v[176:177] op_sel_hi:[1,0]
	v_cvt_pk_fp8_f32 v157, v23, v25
	v_pk_fma_f32 v[158:159], v[10:11], v[172:173], v[158:159] op_sel_hi:[1,0,1]
	v_pk_mul_f32 v[154:155], v[154:155], v[176:177] op_sel_hi:[1,0]
	v_med3_f32 v19, v158, s67, v171
	v_pk_fma_f32 v[154:155], v[14:15], v[172:173], v[154:155] op_sel_hi:[1,0,1]
	v_med3_f32 v21, v159, s67, v171
	v_pk_mul_f32 v[148:149], v[148:149], v[176:177] op_sel_hi:[1,0]
	v_cvt_pk_fp8_f32 v156, v19, v21 op_sel:[0,0,1]
	v_med3_f32 v19, v154, s67, v171
	v_med3_f32 v21, v155, s67, v171
	v_pk_fma_f32 v[148:149], v[0:1], v[172:173], v[148:149] op_sel_hi:[1,0,1]
	v_pk_mul_f32 v[144:145], v[144:145], v[176:177] op_sel_hi:[1,0]
	v_cvt_pk_fp8_f32 v157, v19, v21 op_sel:[0,0,1]
	v_pk_fma_f32 v[144:145], v[4:5], v[172:173], v[144:145] op_sel_hi:[1,0,1]
	v_med3_f32 v19, v148, s67, v171
	v_med3_f32 v21, v149, s67, v171
	v_cvt_pk_fp8_f32 v148, v19, v21
	v_med3_f32 v23, v144, s67, v171
	v_med3_f32 v25, v145, s67, v171
	v_pk_mul_f32 v[150:151], v[150:151], v[176:177] op_sel_hi:[1,0]
	v_cvt_pk_fp8_f32 v149, v23, v25
	v_pk_fma_f32 v[150:151], v[2:3], v[172:173], v[150:151] op_sel_hi:[1,0,1]
	v_pk_mul_f32 v[146:147], v[146:147], v[176:177] op_sel_hi:[1,0]
	v_med3_f32 v19, v150, s67, v171
	v_pk_fma_f32 v[146:147], v[6:7], v[172:173], v[146:147] op_sel_hi:[1,0,1]
	v_med3_f32 v21, v151, s67, v171
	s_or_b32 s4, s4, s53
	v_cvt_pk_fp8_f32 v148, v19, v21 op_sel:[0,0,1]
	v_med3_f32 v19, v146, s67, v171
	v_med3_f32 v21, v147, s67, v171
	v_add_u32_e32 v16, s4, v16
	v_cvt_pk_fp8_f32 v149, v19, v21 op_sel:[0,0,1]
	v_ashrrev_i32_e32 v17, 31, v16
	v_lshl_add_u64 v[144:145], s[10:11], 0, v[178:179]
	v_lshl_add_u64 v[144:145], v[144:145], 0, v[16:17]
	global_store_dwordx2 v[144:145], v[156:157], off
	global_store_dwordx2 v[144:145], v[148:149], off offset:128
	v_mul_f32_e32 v144, 0x3b800000, v174
	v_pk_mul_f32 v[140:141], v[140:141], v[144:145] op_sel_hi:[1,0]
	v_pk_mul_f32 v[136:137], v[136:137], v[144:145] op_sel_hi:[1,0]
	v_pk_fma_f32 v[140:141], v[8:9], v[174:175], v[140:141] op_sel_hi:[1,0,1]
	v_pk_fma_f32 v[136:137], v[12:13], v[174:175], v[136:137] op_sel_hi:[1,0,1]
	v_med3_f32 v19, v140, s67, v171
	v_med3_f32 v21, v141, s67, v171
	v_cvt_pk_fp8_f32 v140, v19, v21
	v_med3_f32 v23, v136, s67, v171
	v_med3_f32 v25, v137, s67, v171
	v_pk_mul_f32 v[142:143], v[142:143], v[144:145] op_sel_hi:[1,0]
	v_cvt_pk_fp8_f32 v141, v23, v25
	v_pk_fma_f32 v[142:143], v[10:11], v[174:175], v[142:143] op_sel_hi:[1,0,1]
	v_pk_mul_f32 v[138:139], v[138:139], v[144:145] op_sel_hi:[1,0]
	v_med3_f32 v19, v142, s67, v171
	v_pk_fma_f32 v[138:139], v[14:15], v[174:175], v[138:139] op_sel_hi:[1,0,1]
	v_med3_f32 v21, v143, s67, v171
	v_pk_mul_f32 v[132:133], v[132:133], v[144:145] op_sel_hi:[1,0]
	v_cvt_pk_fp8_f32 v140, v19, v21 op_sel:[0,0,1]
	v_med3_f32 v19, v138, s67, v171
	v_med3_f32 v21, v139, s67, v171
	v_pk_fma_f32 v[132:133], v[0:1], v[174:175], v[132:133] op_sel_hi:[1,0,1]
	v_pk_mul_f32 v[128:129], v[128:129], v[144:145] op_sel_hi:[1,0]
	v_cvt_pk_fp8_f32 v141, v19, v21 op_sel:[0,0,1]
	v_pk_fma_f32 v[128:129], v[4:5], v[174:175], v[128:129] op_sel_hi:[1,0,1]
	v_med3_f32 v19, v132, s67, v171
	v_med3_f32 v21, v133, s67, v171
	v_cvt_pk_fp8_f32 v132, v19, v21
	v_med3_f32 v23, v128, s67, v171
	v_med3_f32 v25, v129, s67, v171
	v_pk_mul_f32 v[134:135], v[134:135], v[144:145] op_sel_hi:[1,0]
	v_cvt_pk_fp8_f32 v133, v23, v25
	v_pk_fma_f32 v[134:135], v[2:3], v[174:175], v[134:135] op_sel_hi:[1,0,1]
	v_pk_mul_f32 v[130:131], v[130:131], v[144:145] op_sel_hi:[1,0]
	v_add_u32_e32 v146, 16, v20
	v_pk_fma_f32 v[130:131], v[6:7], v[174:175], v[130:131] op_sel_hi:[1,0,1]
	v_med3_f32 v19, v134, s67, v171
	v_med3_f32 v21, v135, s67, v171
	v_ashrrev_i32_e32 v147, 31, v146
	v_cvt_pk_fp8_f32 v132, v19, v21 op_sel:[0,0,1]
	v_med3_f32 v19, v130, s67, v171
	v_med3_f32 v21, v131, s67, v171
	v_lshlrev_b64 v[146:147], 10, v[146:147]
	v_cvt_pk_fp8_f32 v133, v19, v21 op_sel:[0,0,1]
	v_lshl_add_u64 v[128:129], s[10:11], 0, v[146:147]
	v_lshl_add_u64 v[128:129], v[128:129], 0, v[16:17]
	global_store_dwordx2 v[128:129], v[140:141], off
	global_store_dwordx2 v[128:129], v[132:133], off offset:128
	v_mul_f32_e32 v128, 0x3b800000, v30
	v_pk_mul_f32 v[124:125], v[124:125], v[128:129] op_sel_hi:[1,0]
	v_pk_mul_f32 v[120:121], v[120:121], v[128:129] op_sel_hi:[1,0]
	s_waitcnt lgkmcnt(0)
	v_pk_fma_f32 v[124:125], v[8:9], v[30:31], v[124:125] op_sel_hi:[1,0,1]
	v_pk_fma_f32 v[120:121], v[12:13], v[30:31], v[120:121] op_sel_hi:[1,0,1]
	v_med3_f32 v19, v124, s67, v171
	v_med3_f32 v21, v125, s67, v171
	v_cvt_pk_fp8_f32 v124, v19, v21
	v_med3_f32 v23, v120, s67, v171
	v_med3_f32 v25, v121, s67, v171
	v_pk_mul_f32 v[126:127], v[126:127], v[128:129] op_sel_hi:[1,0]
	v_cvt_pk_fp8_f32 v125, v23, v25
	v_pk_fma_f32 v[126:127], v[10:11], v[30:31], v[126:127] op_sel_hi:[1,0,1]
	v_pk_mul_f32 v[122:123], v[122:123], v[128:129] op_sel_hi:[1,0]
	v_cmp_gt_i32_e32 vcc, s15, v18
	v_add_u32_e32 v18, s13, v27
	v_pk_fma_f32 v[122:123], v[14:15], v[30:31], v[122:123] op_sel_hi:[1,0,1]
	v_med3_f32 v19, v126, s67, v171
	v_med3_f32 v21, v127, s67, v171
	v_pk_mul_f32 v[116:117], v[116:117], v[128:129] op_sel_hi:[1,0]
	v_cndmask_b32_e32 v22, 0, v29, vcc
	v_cmp_gt_i32_e32 vcc, s15, v18
	v_cvt_pk_fp8_f32 v124, v19, v21 op_sel:[0,0,1]
	v_med3_f32 v19, v122, s67, v171
	v_med3_f32 v21, v123, s67, v171
	v_pk_mul_f32 v[118:119], v[118:119], v[128:129] op_sel_hi:[1,0]
	v_pk_fma_f32 v[116:117], v[0:1], v[30:31], v[116:117] op_sel_hi:[1,0,1]
	v_pk_mul_f32 v[112:113], v[112:113], v[128:129] op_sel_hi:[1,0]
	v_pk_mul_f32 v[114:115], v[114:115], v[128:129] op_sel_hi:[1,0]
	v_cndmask_b32_e32 v18, 0, v31, vcc
	v_cvt_pk_fp8_f32 v125, v19, v21 op_sel:[0,0,1]
	v_pk_fma_f32 v[118:119], v[2:3], v[30:31], v[118:119] op_sel_hi:[1,0,1]
	v_pk_fma_f32 v[114:115], v[6:7], v[30:31], v[114:115] op_sel_hi:[1,0,1]
	v_pk_fma_f32 v[30:31], v[4:5], v[30:31], v[112:113] op_sel_hi:[1,0,1]
	v_med3_f32 v19, v116, s67, v171
	v_med3_f32 v21, v117, s67, v171
	v_cvt_pk_fp8_f32 v112, v19, v21
	v_med3_f32 v23, v30, s67, v171
	v_med3_f32 v25, v31, s67, v171
	v_cvt_pk_fp8_f32 v113, v23, v25
	v_add_u32_e32 v130, 32, v20
	v_med3_f32 v19, v118, s67, v171
	v_med3_f32 v21, v119, s67, v171
	v_ashrrev_i32_e32 v131, 31, v130
	v_cvt_pk_fp8_f32 v112, v19, v21 op_sel:[0,0,1]
	v_med3_f32 v19, v114, s67, v171
	v_med3_f32 v21, v115, s67, v171
	v_lshlrev_b64 v[130:131], 10, v[130:131]
	v_cvt_pk_fp8_f32 v113, v19, v21 op_sel:[0,0,1]
	v_lshl_add_u64 v[30:31], s[10:11], 0, v[130:131]
	v_lshl_add_u64 v[30:31], v[30:31], 0, v[16:17]
	global_store_dwordx2 v[30:31], v[124:125], off
	global_store_dwordx2 v[30:31], v[112:113], off offset:128
	v_mul_f32_e32 v30, 0x3b800000, v28
	v_pk_mul_f32 v[108:109], v[108:109], v[30:31] op_sel_hi:[1,0]
	v_pk_mul_f32 v[104:105], v[104:105], v[30:31] op_sel_hi:[1,0]
	v_pk_fma_f32 v[108:109], v[8:9], v[28:29], v[108:109] op_sel_hi:[1,0,1]
	v_pk_fma_f32 v[104:105], v[12:13], v[28:29], v[104:105] op_sel_hi:[1,0,1]
	v_med3_f32 v19, v108, s67, v171
	v_med3_f32 v21, v109, s67, v171
	v_cvt_pk_fp8_f32 v108, v19, v21
	v_med3_f32 v23, v104, s67, v171
	v_med3_f32 v25, v105, s67, v171
	v_pk_mul_f32 v[110:111], v[110:111], v[30:31] op_sel_hi:[1,0]
	v_cvt_pk_fp8_f32 v109, v23, v25
	v_pk_fma_f32 v[110:111], v[10:11], v[28:29], v[110:111] op_sel_hi:[1,0,1]
	v_pk_mul_f32 v[106:107], v[106:107], v[30:31] op_sel_hi:[1,0]
	v_med3_f32 v19, v110, s67, v171
	v_pk_fma_f32 v[106:107], v[14:15], v[28:29], v[106:107] op_sel_hi:[1,0,1]
	v_med3_f32 v21, v111, s67, v171
	v_pk_mul_f32 v[100:101], v[100:101], v[30:31] op_sel_hi:[1,0]
	v_cvt_pk_fp8_f32 v108, v19, v21 op_sel:[0,0,1]
	v_med3_f32 v19, v106, s67, v171
	v_med3_f32 v21, v107, s67, v171
	v_pk_mul_f32 v[102:103], v[102:103], v[30:31] op_sel_hi:[1,0]
	v_pk_fma_f32 v[100:101], v[0:1], v[28:29], v[100:101] op_sel_hi:[1,0,1]
	v_pk_mul_f32 v[96:97], v[96:97], v[30:31] op_sel_hi:[1,0]
	v_pk_mul_f32 v[30:31], v[98:99], v[30:31] op_sel_hi:[1,0]
	v_cvt_pk_fp8_f32 v109, v19, v21 op_sel:[0,0,1]
	v_pk_fma_f32 v[102:103], v[2:3], v[28:29], v[102:103] op_sel_hi:[1,0,1]
	v_pk_fma_f32 v[30:31], v[6:7], v[28:29], v[30:31] op_sel_hi:[1,0,1]
	v_pk_fma_f32 v[28:29], v[4:5], v[28:29], v[96:97] op_sel_hi:[1,0,1]
	v_med3_f32 v19, v100, s67, v171
	v_med3_f32 v21, v101, s67, v171
	v_cvt_pk_fp8_f32 v96, v19, v21
	v_med3_f32 v23, v28, s67, v171
	v_med3_f32 v25, v29, s67, v171
	v_med3_f32 v19, v102, s67, v171
	v_med3_f32 v21, v103, s67, v171
	v_cvt_pk_fp8_f32 v97, v23, v25
	v_cvt_pk_fp8_f32 v96, v19, v21 op_sel:[0,0,1]
	v_med3_f32 v19, v30, s67, v171
	v_mul_f32_e32 v30, 0x3b800000, v26
	v_pk_mul_f32 v[92:93], v[92:93], v[30:31] op_sel_hi:[1,0]
	v_med3_f32 v21, v31, s67, v171
	v_pk_fma_f32 v[92:93], v[8:9], v[26:27], v[92:93] op_sel_hi:[1,0,1]
	v_pk_mul_f32 v[88:89], v[88:89], v[30:31] op_sel_hi:[1,0]
	v_cvt_pk_fp8_f32 v97, v19, v21 op_sel:[0,0,1]
	v_pk_fma_f32 v[88:89], v[12:13], v[26:27], v[88:89] op_sel_hi:[1,0,1]
	v_med3_f32 v19, v92, s67, v171
	v_med3_f32 v21, v93, s67, v171
	v_cvt_pk_fp8_f32 v92, v19, v21
	v_med3_f32 v23, v88, s67, v171
	v_med3_f32 v25, v89, s67, v171
	v_pk_mul_f32 v[94:95], v[94:95], v[30:31] op_sel_hi:[1,0]
	v_cvt_pk_fp8_f32 v93, v23, v25
	v_pk_fma_f32 v[94:95], v[10:11], v[26:27], v[94:95] op_sel_hi:[1,0,1]
	v_pk_mul_f32 v[90:91], v[90:91], v[30:31] op_sel_hi:[1,0]
	v_med3_f32 v19, v94, s67, v171
	v_pk_fma_f32 v[90:91], v[14:15], v[26:27], v[90:91] op_sel_hi:[1,0,1]
	v_med3_f32 v21, v95, s67, v171
	v_pk_mul_f32 v[84:85], v[84:85], v[30:31] op_sel_hi:[1,0]
	v_add_u32_e32 v112, 48, v20
	v_cvt_pk_fp8_f32 v92, v19, v21 op_sel:[0,0,1]
	v_med3_f32 v19, v90, s67, v171
	v_med3_f32 v21, v91, s67, v171
	v_pk_mul_f32 v[86:87], v[86:87], v[30:31] op_sel_hi:[1,0]
	v_pk_fma_f32 v[84:85], v[0:1], v[26:27], v[84:85] op_sel_hi:[1,0,1]
	v_pk_mul_f32 v[80:81], v[80:81], v[30:31] op_sel_hi:[1,0]
	v_pk_mul_f32 v[30:31], v[82:83], v[30:31] op_sel_hi:[1,0]
	v_ashrrev_i32_e32 v113, 31, v112
	v_cvt_pk_fp8_f32 v93, v19, v21 op_sel:[0,0,1]
	v_pk_fma_f32 v[86:87], v[2:3], v[26:27], v[86:87] op_sel_hi:[1,0,1]
	v_pk_fma_f32 v[30:31], v[6:7], v[26:27], v[30:31] op_sel_hi:[1,0,1]
	v_pk_fma_f32 v[26:27], v[4:5], v[26:27], v[80:81] op_sel_hi:[1,0,1]
	v_med3_f32 v19, v84, s67, v171
	v_med3_f32 v21, v85, s67, v171
	v_lshlrev_b64 v[112:113], 10, v[112:113]
	v_cvt_pk_fp8_f32 v80, v19, v21
	v_med3_f32 v23, v26, s67, v171
	v_med3_f32 v25, v27, s67, v171
	v_lshl_add_u64 v[28:29], s[10:11], 0, v[112:113]
	v_cvt_pk_fp8_f32 v81, v23, v25
	v_lshl_add_u64 v[28:29], v[28:29], 0, v[16:17]
	global_store_dwordx2 v[28:29], v[108:109], off
	global_store_dwordx2 v[28:29], v[96:97], off offset:128
	v_add_u32_e32 v28, 0x80, v20
	v_med3_f32 v19, v86, s67, v171
	v_med3_f32 v21, v87, s67, v171
	v_ashrrev_i32_e32 v29, 31, v28
	v_cvt_pk_fp8_f32 v80, v19, v21 op_sel:[0,0,1]
	v_med3_f32 v19, v30, s67, v171
	v_med3_f32 v21, v31, s67, v171
	v_lshlrev_b64 v[28:29], 10, v[28:29]
	v_cvt_pk_fp8_f32 v81, v19, v21 op_sel:[0,0,1]
	v_lshl_add_u64 v[26:27], s[10:11], 0, v[28:29]
	v_lshl_add_u64 v[26:27], v[26:27], 0, v[16:17]
	global_store_dwordx2 v[26:27], v[92:93], off
	global_store_dwordx2 v[26:27], v[80:81], off offset:128
	v_mul_f32_e32 v26, 0x3b800000, v24
	v_pk_mul_f32 v[30:31], v[76:77], v[26:27] op_sel_hi:[1,0]
	v_pk_mul_f32 v[72:73], v[72:73], v[26:27] op_sel_hi:[1,0]
	v_pk_fma_f32 v[30:31], v[8:9], v[24:25], v[30:31] op_sel_hi:[1,0,1]
	v_pk_mul_f32 v[76:77], v[78:79], v[26:27] op_sel_hi:[1,0]
	v_pk_mul_f32 v[74:75], v[74:75], v[26:27] op_sel_hi:[1,0]
	v_pk_fma_f32 v[72:73], v[12:13], v[24:25], v[72:73] op_sel_hi:[1,0,1]
	v_med3_f32 v19, v30, s67, v171
	v_med3_f32 v21, v31, s67, v171
	v_pk_fma_f32 v[76:77], v[10:11], v[24:25], v[76:77] op_sel_hi:[1,0,1]
	v_pk_fma_f32 v[74:75], v[14:15], v[24:25], v[74:75] op_sel_hi:[1,0,1]
	v_cvt_pk_fp8_f32 v30, v19, v21
	v_med3_f32 v23, v72, s67, v171
	v_med3_f32 v25, v73, s67, v171
	v_cvt_pk_fp8_f32 v31, v23, v25
	v_med3_f32 v19, v76, s67, v171
	v_med3_f32 v21, v77, s67, v171
	v_pk_mul_f32 v[68:69], v[68:69], v[26:27] op_sel_hi:[1,0]
	v_cvt_pk_fp8_f32 v30, v19, v21 op_sel:[0,0,1]
	v_med3_f32 v19, v74, s67, v171
	v_med3_f32 v21, v75, s67, v171
	v_pk_mul_f32 v[70:71], v[70:71], v[26:27] op_sel_hi:[1,0]
	v_pk_fma_f32 v[68:69], v[0:1], v[24:25], v[68:69] op_sel_hi:[1,0,1]
	v_pk_mul_f32 v[64:65], v[64:65], v[26:27] op_sel_hi:[1,0]
	v_pk_mul_f32 v[26:27], v[66:67], v[26:27] op_sel_hi:[1,0]
	v_cvt_pk_fp8_f32 v31, v19, v21 op_sel:[0,0,1]
	v_pk_fma_f32 v[70:71], v[2:3], v[24:25], v[70:71] op_sel_hi:[1,0,1]
	v_pk_fma_f32 v[26:27], v[6:7], v[24:25], v[26:27] op_sel_hi:[1,0,1]
	v_pk_fma_f32 v[24:25], v[4:5], v[24:25], v[64:65] op_sel_hi:[1,0,1]
	v_med3_f32 v19, v68, s67, v171
	v_med3_f32 v21, v69, s67, v171
	v_cvt_pk_fp8_f32 v64, v19, v21
	v_med3_f32 v23, v24, s67, v171
	v_med3_f32 v24, v25, s67, v171
	v_cvt_pk_fp8_f32 v65, v23, v24
	v_add_u32_e32 v28, 0x90, v20
	v_med3_f32 v19, v70, s67, v171
	v_med3_f32 v21, v71, s67, v171
	v_ashrrev_i32_e32 v29, 31, v28
	v_cvt_pk_fp8_f32 v64, v19, v21 op_sel:[0,0,1]
	v_med3_f32 v19, v26, s67, v171
	v_med3_f32 v21, v27, s67, v171
	v_lshlrev_b64 v[28:29], 10, v[28:29]
	v_cvt_pk_fp8_f32 v65, v19, v21 op_sel:[0,0,1]
	v_lshl_add_u64 v[24:25], s[10:11], 0, v[28:29]
	v_lshl_add_u64 v[24:25], v[24:25], 0, v[16:17]
	global_store_dwordx2 v[24:25], v[30:31], off
	global_store_dwordx2 v[24:25], v[64:65], off offset:128
	v_mul_f32_e32 v24, 0x3b800000, v22
	v_pk_mul_f32 v[28:29], v[60:61], v[24:25] op_sel_hi:[1,0]
	v_pk_mul_f32 v[56:57], v[56:57], v[24:25] op_sel_hi:[1,0]
	v_pk_fma_f32 v[28:29], v[8:9], v[22:23], v[28:29] op_sel_hi:[1,0,1]
	v_pk_mul_f32 v[30:31], v[62:63], v[24:25] op_sel_hi:[1,0]
	v_pk_mul_f32 v[58:59], v[58:59], v[24:25] op_sel_hi:[1,0]
	v_pk_fma_f32 v[56:57], v[12:13], v[22:23], v[56:57] op_sel_hi:[1,0,1]
	v_med3_f32 v19, v28, s67, v171
	v_med3_f32 v21, v29, s67, v171
	v_pk_fma_f32 v[30:31], v[10:11], v[22:23], v[30:31] op_sel_hi:[1,0,1]
	v_pk_fma_f32 v[58:59], v[14:15], v[22:23], v[58:59] op_sel_hi:[1,0,1]
	v_cvt_pk_fp8_f32 v28, v19, v21
	v_med3_f32 v23, v56, s67, v171
	v_med3_f32 v25, v57, s67, v171
	v_cvt_pk_fp8_f32 v29, v23, v25
	v_med3_f32 v19, v30, s67, v171
	v_med3_f32 v21, v31, s67, v171
	v_pk_mul_f32 v[30:31], v[52:53], v[24:25] op_sel_hi:[1,0]
	v_cvt_pk_fp8_f32 v28, v19, v21 op_sel:[0,0,1]
	v_med3_f32 v19, v58, s67, v171
	v_med3_f32 v21, v59, s67, v171
	v_pk_mul_f32 v[52:53], v[54:55], v[24:25] op_sel_hi:[1,0]
	v_pk_fma_f32 v[30:31], v[0:1], v[22:23], v[30:31] op_sel_hi:[1,0,1]
	v_pk_mul_f32 v[48:49], v[48:49], v[24:25] op_sel_hi:[1,0]
	v_pk_mul_f32 v[24:25], v[50:51], v[24:25] op_sel_hi:[1,0]
	v_cvt_pk_fp8_f32 v29, v19, v21 op_sel:[0,0,1]
	v_pk_fma_f32 v[52:53], v[2:3], v[22:23], v[52:53] op_sel_hi:[1,0,1]
	v_pk_fma_f32 v[24:25], v[6:7], v[22:23], v[24:25] op_sel_hi:[1,0,1]
	v_pk_fma_f32 v[22:23], v[4:5], v[22:23], v[48:49] op_sel_hi:[1,0,1]
	v_med3_f32 v19, v30, s67, v171
	v_med3_f32 v21, v31, s67, v171
	v_cvt_pk_fp8_f32 v30, v19, v21
	v_med3_f32 v22, v22, s67, v171
	v_med3_f32 v23, v23, s67, v171
	v_cvt_pk_fp8_f32 v31, v22, v23
	v_add_u32_e32 v26, 0xa0, v20
	v_med3_f32 v19, v52, s67, v171
	v_med3_f32 v21, v53, s67, v171
	v_ashrrev_i32_e32 v27, 31, v26
	v_cvt_pk_fp8_f32 v30, v19, v21 op_sel:[0,0,1]
	v_med3_f32 v19, v24, s67, v171
	v_med3_f32 v21, v25, s67, v171
	v_lshlrev_b64 v[26:27], 10, v[26:27]
	v_cvt_pk_fp8_f32 v31, v19, v21 op_sel:[0,0,1]
	v_lshl_add_u64 v[22:23], s[10:11], 0, v[26:27]
	v_lshl_add_u64 v[22:23], v[22:23], 0, v[16:17]
	global_store_dwordx2 v[22:23], v[28:29], off
	global_store_dwordx2 v[22:23], v[30:31], off offset:128
	v_mul_f32_e32 v22, 0x3b800000, v18
	v_pk_mul_f32 v[24:25], v[44:45], v[22:23] op_sel_hi:[1,0]
	v_pk_mul_f32 v[26:27], v[46:47], v[22:23] op_sel_hi:[1,0]
	v_pk_fma_f32 v[8:9], v[8:9], v[18:19], v[24:25] op_sel_hi:[1,0,1]
	v_pk_fma_f32 v[10:11], v[10:11], v[18:19], v[26:27] op_sel_hi:[1,0,1]
	v_pk_mul_f32 v[24:25], v[40:41], v[22:23] op_sel_hi:[1,0]
	v_pk_mul_f32 v[26:27], v[42:43], v[22:23] op_sel_hi:[1,0]
	v_pk_fma_f32 v[12:13], v[12:13], v[18:19], v[24:25] op_sel_hi:[1,0,1]
	v_pk_fma_f32 v[14:15], v[14:15], v[18:19], v[26:27] op_sel_hi:[1,0,1]
	v_med3_f32 v19, v8, s67, v171
	v_med3_f32 v9, v9, s67, v171
	v_cvt_pk_fp8_f32 v8, v19, v9
	v_med3_f32 v12, v12, s67, v171
	v_med3_f32 v13, v13, s67, v171
	v_cvt_pk_fp8_f32 v9, v12, v13
	v_med3_f32 v10, v10, s67, v171
	v_med3_f32 v11, v11, s67, v171
	v_cvt_pk_fp8_f32 v8, v10, v11 op_sel:[0,0,1]
	v_med3_f32 v10, v14, s67, v171
	v_med3_f32 v11, v15, s67, v171
	v_cvt_pk_fp8_f32 v9, v10, v11 op_sel:[0,0,1]
	v_pk_mul_f32 v[10:11], v[36:37], v[22:23] op_sel_hi:[1,0]
	v_pk_mul_f32 v[12:13], v[38:39], v[22:23] op_sel_hi:[1,0]
	v_pk_fma_f32 v[0:1], v[0:1], v[18:19], v[10:11] op_sel_hi:[1,0,1]
	v_pk_mul_f32 v[10:11], v[32:33], v[22:23] op_sel_hi:[1,0]
	v_med3_f32 v1, v1, s67, v171
	v_pk_fma_f32 v[4:5], v[4:5], v[18:19], v[10:11] op_sel_hi:[1,0,1]
	v_med3_f32 v10, v0, s67, v171
	v_mov_b32_e32 v0, 0
	v_cvt_pk_fp8_f32 v0, v10, v1
	v_med3_f32 v4, v4, s67, v171
	v_med3_f32 v5, v5, s67, v171
	v_cvt_pk_fp8_f32 v1, v4, v5
	v_pk_fma_f32 v[2:3], v[2:3], v[18:19], v[12:13] op_sel_hi:[1,0,1]
	v_pk_mul_f32 v[12:13], v[34:35], v[22:23] op_sel_hi:[1,0]
	v_add_u32_e32 v20, 0xb0, v20
	v_pk_fma_f32 v[6:7], v[6:7], v[18:19], v[12:13] op_sel_hi:[1,0,1]
	v_med3_f32 v2, v2, s67, v171
	v_med3_f32 v3, v3, s67, v171
	v_ashrrev_i32_e32 v21, 31, v20
	v_cvt_pk_fp8_f32 v0, v2, v3 op_sel:[0,0,1]
	v_med3_f32 v2, v6, s67, v171
	v_med3_f32 v3, v7, s67, v171
	v_lshlrev_b64 v[20:21], 10, v[20:21]
	v_cvt_pk_fp8_f32 v1, v2, v3 op_sel:[0,0,1]
	v_lshl_add_u64 v[2:3], s[10:11], 0, v[20:21]
	v_lshl_add_u64 v[2:3], v[2:3], 0, v[16:17]
	s_and_b64 vcc, exec, s[0:1]
	s_mov_b64 s[0:1], -1
	global_store_dwordx2 v[2:3], v[8:9], off
	global_store_dwordx2 v[2:3], v[0:1], off offset:128
	s_cbranch_vccnz .LBB0_2111
	s_andn2_b64 vcc, exec, s[6:7]
	s_cbranch_vccnz .LBB0_2110
	s_barrier
	s_branch .LBB0_2110
